# v057
# speedup vs baseline: 1.1289x; 1.0110x over previous
.LBB2_45:
	s_and_b64 vcc, exec, s[28:29]
	s_cbranch_vccnz .Lmy_epi_last
	s_cmp_eq_u32 s30, 7
	s_cbranch_scc1 .Lmy_epi_nl7
	v_exp_f32_e32 v120, v120
	v_exp_f32_e32 v121, v121
	v_exp_f32_e32 v122, v122
	v_pk_add_f32 v[120:121], v[120:121], 1.0 op_sel_hi:[1,0]
	v_exp_f32_e32 v123, v123
	v_exp_f32_e32 v124, v124
	v_pk_add_f32 v[122:123], v[122:123], 1.0 op_sel_hi:[1,0]
	v_exp_f32_e32 v125, v125
	v_exp_f32_e32 v126, v126
	v_pk_add_f32 v[124:125], v[124:125], 1.0 op_sel_hi:[1,0]
	v_exp_f32_e32 v127, v127
	v_exp_f32_e32 v116, v116
	v_pk_add_f32 v[126:127], v[126:127], 1.0 op_sel_hi:[1,0]
	v_exp_f32_e32 v117, v117
	v_pk_mul_f32 v[120:121], v[120:121], v[124:125]
	v_exp_f32_e32 v118, v118
	v_pk_mul_f32 v[122:123], v[122:123], v[126:127]
	v_exp_f32_e32 v119, v119
	v_pk_add_f32 v[124:125], v[124:125], 2.0 op_sel_hi:[1,0] neg_lo:[1,0] neg_hi:[1,0]
	v_pk_add_f32 v[116:117], v[116:117], 1.0 op_sel_hi:[1,0]
	v_pk_add_f32 v[126:127], v[126:127], 2.0 op_sel_hi:[1,0] neg_lo:[1,0] neg_hi:[1,0]
	v_pk_add_f32 v[118:119], v[118:119], 1.0 op_sel_hi:[1,0]
	v_pk_mul_f32 v[124:125], v[124:125], v[116:117]
	v_pk_mul_f32 v[116:117], v[116:117], v[120:121]
	v_pk_mul_f32 v[126:127], v[126:127], v[118:119]
	v_pk_mul_f32 v[118:119], v[118:119], v[122:123]
	v_rcp_f32_e32 v116, v116
	v_rcp_f32_e32 v117, v117
	v_rcp_f32_e32 v118, v118
	v_rcp_f32_e32 v119, v119
	s_waitcnt lgkmcnt(3)
	v_pk_fma_f32 v[124:125], v[172:173], v[120:121], v[124:125]
	v_pk_fma_f32 v[126:127], v[174:175], v[122:123], v[126:127]
	v_pk_mul_f32 v[116:117], v[116:117], v[124:125]
	v_pk_mul_f32 v[118:119], v[118:119], v[126:127]
	global_store_dwordx4 v[176:177], v[116:119], off nt
	s_nop 1
	v_pk_mul_f32 v[116:117], v[116:117], s[96:97] op_sel_hi:[1,0]
	v_pk_mul_f32 v[118:119], v[118:119], s[96:97] op_sel_hi:[1,0]
	v_exp_f32_e32 v112, v112
	v_exp_f32_e32 v113, v113
	v_exp_f32_e32 v114, v114
	v_pk_fma_f32 v[112:113], v[112:113], s[98:99], s[98:99] op_sel_hi:[1,0,0]
	v_exp_f32_e32 v115, v115
	v_exp_f32_e32 v116, v116
	v_pk_fma_f32 v[114:115], v[114:115], s[98:99], s[98:99] op_sel_hi:[1,0,0]
	v_exp_f32_e32 v117, v117
	v_exp_f32_e32 v118, v118
	v_pk_add_f32 v[116:117], v[116:117], 1.0 op_sel_hi:[1,0]
	v_exp_f32_e32 v119, v119
	v_pk_mul_f32 v[112:113], v[112:113], v[116:117]
	v_rcp_f32_e32 v112, v112
	v_pk_add_f32 v[118:119], v[118:119], 1.0 op_sel_hi:[1,0]
	v_rcp_f32_e32 v113, v113
	v_pk_mul_f32 v[114:115], v[114:115], v[118:119]
	v_pk_add_f32 v[116:117], v[116:117], 2.0 op_sel_hi:[1,0] neg_lo:[1,0] neg_hi:[1,0]
	v_rcp_f32_e32 v114, v114
	v_rcp_f32_e32 v115, v115
	v_pk_add_f32 v[118:119], v[118:119], 2.0 op_sel_hi:[1,0] neg_lo:[1,0] neg_hi:[1,0]
	v_pk_mul_f32 v[112:113], v[112:113], v[116:117]
	v_pk_mul_f32 v[114:115], v[114:115], v[118:119]
	v_cvt_pk_fp8_f32 v124, v112, v113
	s_add_u32 s0, s8, s27
	s_addc_u32 s1, s9, 0
	s_ashr_i32 s35, s34, 31
	s_lshl_b64 s[34:35], s[34:35], 21
	v_ashrrev_i32_e32 v209, 31, v208
	s_add_u32 s36, s73, s34
	v_lshrrev_b32_e32 v126, 4, v210
	v_and_b32_e32 v127, 15, v210
	v_lshl_or_b32 v126, v126, 8, v127
	v_and_b32_e32 v127, 15, v208
	v_mul_u32_u24_e32 v127, 0x3f0, v127
	v_sub_u32_e32 v126, v126, v127
	v_ashrrev_i32_e32 v127, 31, v126
	v_lshl_add_u64 v[122:123], s[0:1], 0, v[126:127]
	v_cvt_pk_fp8_f32 v124, v114, v115 op_sel:[0,0,1]
	v_lshlrev_b64 v[116:117], 10, v[208:209]
	s_addc_u32 s37, s74, s35
	v_lshl_add_u64 v[118:119], v[122:123], 0, v[116:117]
	global_store_dword v[118:119], v124, off
	s_cmp_eq_u32 s30, 7
	s_cselect_b64 s[34:35], -1, 0
	s_cmp_lg_u32 s30, 7
	v_lshrrev_b32_e32 v126, 4, v210
	v_lshlrev_b32_e32 v126, 9, v126
	v_and_b32_e32 v127, 15, v210
	v_lshl_or_b32 v126, v127, 1, v126
	v_and_b32_e32 v127, 15, v208
	v_mul_u32_u24_e32 v127, 0x7e0, v127
	v_sub_u32_e32 v126, v126, v127
	v_ashrrev_i32_e32 v127, 31, v126
	v_lshl_add_u64 v[120:121], s[36:37], 0, v[126:127]
	v_exp_f32_e32 v104, v104
	v_exp_f32_e32 v105, v105
	v_exp_f32_e32 v106, v106
	v_pk_add_f32 v[104:105], v[104:105], 1.0 op_sel_hi:[1,0]
	v_exp_f32_e32 v107, v107
	v_exp_f32_e32 v108, v108
	v_pk_add_f32 v[106:107], v[106:107], 1.0 op_sel_hi:[1,0]
	v_exp_f32_e32 v109, v109
	v_exp_f32_e32 v110, v110
	v_pk_add_f32 v[108:109], v[108:109], 1.0 op_sel_hi:[1,0]
	v_exp_f32_e32 v111, v111
	v_exp_f32_e32 v100, v100
	v_pk_add_f32 v[110:111], v[110:111], 1.0 op_sel_hi:[1,0]
	v_exp_f32_e32 v101, v101
	v_pk_mul_f32 v[104:105], v[104:105], v[108:109]
	v_exp_f32_e32 v102, v102
	v_pk_mul_f32 v[106:107], v[106:107], v[110:111]
	v_exp_f32_e32 v103, v103
	v_pk_add_f32 v[108:109], v[108:109], 2.0 op_sel_hi:[1,0] neg_lo:[1,0] neg_hi:[1,0]
	v_pk_add_f32 v[100:101], v[100:101], 1.0 op_sel_hi:[1,0]
	v_pk_add_f32 v[110:111], v[110:111], 2.0 op_sel_hi:[1,0] neg_lo:[1,0] neg_hi:[1,0]
	v_pk_add_f32 v[102:103], v[102:103], 1.0 op_sel_hi:[1,0]
	v_pk_mul_f32 v[108:109], v[108:109], v[100:101]
	v_pk_mul_f32 v[100:101], v[100:101], v[104:105]
	v_pk_mul_f32 v[110:111], v[110:111], v[102:103]
	v_pk_mul_f32 v[102:103], v[102:103], v[106:107]
	v_rcp_f32_e32 v100, v100
	v_rcp_f32_e32 v101, v101
	v_rcp_f32_e32 v102, v102
	v_rcp_f32_e32 v103, v103
	s_waitcnt lgkmcnt(2)
	v_pk_fma_f32 v[108:109], v[168:169], v[104:105], v[108:109]
	v_pk_fma_f32 v[110:111], v[170:171], v[106:107], v[110:111]
	v_lshl_add_u64 v[104:105], v[176:177], 0, s[18:19]
	v_pk_mul_f32 v[100:101], v[100:101], v[108:109]
	v_pk_mul_f32 v[102:103], v[102:103], v[110:111]
	global_store_dwordx4 v[104:105], v[100:103], off nt
	s_nop 1
	v_pk_mul_f32 v[100:101], v[100:101], s[96:97] op_sel_hi:[1,0]
	v_pk_mul_f32 v[102:103], v[102:103], s[96:97] op_sel_hi:[1,0]
	v_exp_f32_e32 v96, v96
	v_exp_f32_e32 v97, v97
	v_exp_f32_e32 v98, v98
	v_pk_fma_f32 v[96:97], v[96:97], s[98:99], s[98:99] op_sel_hi:[1,0,0]
	v_exp_f32_e32 v99, v99
	v_exp_f32_e32 v100, v100
	v_pk_fma_f32 v[98:99], v[98:99], s[98:99], s[98:99] op_sel_hi:[1,0,0]
	v_exp_f32_e32 v101, v101
	v_exp_f32_e32 v102, v102
	v_pk_add_f32 v[100:101], v[100:101], 1.0 op_sel_hi:[1,0]
	v_exp_f32_e32 v103, v103
	v_pk_mul_f32 v[96:97], v[96:97], v[100:101]
	v_rcp_f32_e32 v96, v96
	v_pk_add_f32 v[102:103], v[102:103], 1.0 op_sel_hi:[1,0]
	v_rcp_f32_e32 v97, v97
	v_pk_mul_f32 v[98:99], v[98:99], v[102:103]
	v_pk_add_f32 v[100:101], v[100:101], 2.0 op_sel_hi:[1,0] neg_lo:[1,0] neg_hi:[1,0]
	v_rcp_f32_e32 v98, v98
	v_rcp_f32_e32 v99, v99
	v_pk_add_f32 v[102:103], v[102:103], 2.0 op_sel_hi:[1,0] neg_lo:[1,0] neg_hi:[1,0]
	v_pk_mul_f32 v[96:97], v[96:97], v[100:101]
	v_pk_mul_f32 v[98:99], v[98:99], v[102:103]
	v_cvt_pk_fp8_f32 v104, v96, v97
	v_ashrrev_i32_e32 v207, 31, v206
	v_lshlrev_b64 v[100:101], 10, v[206:207]
	v_lshl_add_u64 v[102:103], v[122:123], 0, v[100:101]
	v_cvt_pk_fp8_f32 v104, v98, v99 op_sel:[0,0,1]
	v_cndmask_b32_e64 v105, 0, 1, s[34:35]
	global_store_dword v[102:103], v104, off
	v_cmp_ne_u32_e64 s[0:1], 1, v105
	v_exp_f32_e32 v88, v88
	v_exp_f32_e32 v89, v89
	v_exp_f32_e32 v90, v90
	v_pk_add_f32 v[88:89], v[88:89], 1.0 op_sel_hi:[1,0]
	v_exp_f32_e32 v91, v91
	v_exp_f32_e32 v92, v92
	v_pk_add_f32 v[90:91], v[90:91], 1.0 op_sel_hi:[1,0]
	v_exp_f32_e32 v93, v93
	v_exp_f32_e32 v94, v94
	v_pk_add_f32 v[92:93], v[92:93], 1.0 op_sel_hi:[1,0]
	v_exp_f32_e32 v95, v95
	v_exp_f32_e32 v84, v84
	v_pk_add_f32 v[94:95], v[94:95], 1.0 op_sel_hi:[1,0]
	v_exp_f32_e32 v85, v85
	v_pk_mul_f32 v[88:89], v[88:89], v[92:93]
	v_exp_f32_e32 v86, v86
	v_pk_mul_f32 v[90:91], v[90:91], v[94:95]
	v_exp_f32_e32 v87, v87
	v_pk_add_f32 v[92:93], v[92:93], 2.0 op_sel_hi:[1,0] neg_lo:[1,0] neg_hi:[1,0]
	v_pk_add_f32 v[84:85], v[84:85], 1.0 op_sel_hi:[1,0]
	v_pk_add_f32 v[94:95], v[94:95], 2.0 op_sel_hi:[1,0] neg_lo:[1,0] neg_hi:[1,0]
	v_pk_add_f32 v[86:87], v[86:87], 1.0 op_sel_hi:[1,0]
	v_pk_mul_f32 v[92:93], v[92:93], v[84:85]
	v_pk_mul_f32 v[84:85], v[84:85], v[88:89]
	v_pk_mul_f32 v[94:95], v[94:95], v[86:87]
	v_pk_mul_f32 v[86:87], v[86:87], v[90:91]
	v_rcp_f32_e32 v84, v84
	v_rcp_f32_e32 v85, v85
	v_rcp_f32_e32 v86, v86
	v_rcp_f32_e32 v87, v87
	s_waitcnt lgkmcnt(1)
	v_pk_fma_f32 v[92:93], v[164:165], v[88:89], v[92:93]
	v_pk_fma_f32 v[94:95], v[166:167], v[90:91], v[94:95]
	v_pk_mul_f32 v[84:85], v[84:85], v[92:93]
	v_pk_mul_f32 v[86:87], v[86:87], v[94:95]
	v_lshl_add_u64 v[88:89], v[176:177], 0, s[12:13]
	global_store_dwordx4 v[88:89], v[84:87], off nt
	s_nop 1
	v_pk_mul_f32 v[84:85], v[84:85], s[96:97] op_sel_hi:[1,0]
	v_pk_mul_f32 v[86:87], v[86:87], s[96:97] op_sel_hi:[1,0]
	v_exp_f32_e32 v80, v80
	v_exp_f32_e32 v81, v81
	v_exp_f32_e32 v82, v82
	v_pk_fma_f32 v[80:81], v[80:81], s[98:99], s[98:99] op_sel_hi:[1,0,0]
	v_exp_f32_e32 v83, v83
	v_exp_f32_e32 v84, v84
	v_pk_fma_f32 v[82:83], v[82:83], s[98:99], s[98:99] op_sel_hi:[1,0,0]
	v_exp_f32_e32 v85, v85
	v_exp_f32_e32 v86, v86
	v_pk_add_f32 v[84:85], v[84:85], 1.0 op_sel_hi:[1,0]
	v_exp_f32_e32 v87, v87
	v_pk_mul_f32 v[80:81], v[80:81], v[84:85]
	v_rcp_f32_e32 v80, v80
	v_pk_add_f32 v[86:87], v[86:87], 1.0 op_sel_hi:[1,0]
	v_rcp_f32_e32 v81, v81
	v_pk_mul_f32 v[82:83], v[82:83], v[86:87]
	v_pk_add_f32 v[84:85], v[84:85], 2.0 op_sel_hi:[1,0] neg_lo:[1,0] neg_hi:[1,0]
	v_rcp_f32_e32 v82, v82
	v_rcp_f32_e32 v83, v83
	v_pk_add_f32 v[86:87], v[86:87], 2.0 op_sel_hi:[1,0] neg_lo:[1,0] neg_hi:[1,0]
	v_pk_mul_f32 v[80:81], v[80:81], v[84:85]
	v_pk_mul_f32 v[82:83], v[82:83], v[86:87]
	v_ashrrev_i32_e32 v205, 31, v204
	v_cvt_pk_fp8_f32 v88, v80, v81
	s_and_b64 vcc, exec, s[0:1]
	v_cvt_pk_fp8_f32 v88, v82, v83 op_sel:[0,0,1]
	v_lshlrev_b64 v[84:85], 10, v[204:205]
	v_lshl_add_u64 v[86:87], v[122:123], 0, v[84:85]
	global_store_dword v[86:87], v88, off
	v_exp_f32_e32 v72, v72
	v_exp_f32_e32 v73, v73
	v_exp_f32_e32 v74, v74
	v_pk_add_f32 v[72:73], v[72:73], 1.0 op_sel_hi:[1,0]
	v_exp_f32_e32 v75, v75
	v_exp_f32_e32 v76, v76
	v_pk_add_f32 v[74:75], v[74:75], 1.0 op_sel_hi:[1,0]
	v_exp_f32_e32 v77, v77
	v_exp_f32_e32 v78, v78
	v_pk_add_f32 v[76:77], v[76:77], 1.0 op_sel_hi:[1,0]
	v_exp_f32_e32 v79, v79
	v_exp_f32_e32 v68, v68
	v_pk_add_f32 v[78:79], v[78:79], 1.0 op_sel_hi:[1,0]
	v_exp_f32_e32 v69, v69
	v_pk_mul_f32 v[72:73], v[72:73], v[76:77]
	v_exp_f32_e32 v70, v70
	v_pk_mul_f32 v[74:75], v[74:75], v[78:79]
	v_exp_f32_e32 v71, v71
	v_pk_add_f32 v[76:77], v[76:77], 2.0 op_sel_hi:[1,0] neg_lo:[1,0] neg_hi:[1,0]
	v_pk_add_f32 v[68:69], v[68:69], 1.0 op_sel_hi:[1,0]
	v_pk_add_f32 v[78:79], v[78:79], 2.0 op_sel_hi:[1,0] neg_lo:[1,0] neg_hi:[1,0]
	v_pk_add_f32 v[70:71], v[70:71], 1.0 op_sel_hi:[1,0]
	v_pk_mul_f32 v[76:77], v[76:77], v[68:69]
	v_pk_mul_f32 v[68:69], v[68:69], v[72:73]
	v_pk_mul_f32 v[78:79], v[78:79], v[70:71]
	v_pk_mul_f32 v[70:71], v[70:71], v[74:75]
	v_rcp_f32_e32 v68, v68
	v_rcp_f32_e32 v69, v69
	v_rcp_f32_e32 v70, v70
	v_rcp_f32_e32 v71, v71
	s_waitcnt lgkmcnt(0)
	v_pk_fma_f32 v[76:77], v[160:161], v[72:73], v[76:77]
	v_pk_fma_f32 v[78:79], v[162:163], v[74:75], v[78:79]
	v_lshl_add_u64 v[72:73], v[176:177], 0, s[20:21]
	v_pk_mul_f32 v[68:69], v[68:69], v[76:77]
	v_pk_mul_f32 v[70:71], v[70:71], v[78:79]
	global_store_dwordx4 v[72:73], v[68:71], off nt
	s_nop 1
	v_pk_mul_f32 v[68:69], v[68:69], s[96:97] op_sel_hi:[1,0]
	v_pk_mul_f32 v[70:71], v[70:71], s[96:97] op_sel_hi:[1,0]
	v_exp_f32_e32 v64, v64
	v_exp_f32_e32 v65, v65
	v_exp_f32_e32 v66, v66
	v_pk_fma_f32 v[64:65], v[64:65], s[98:99], s[98:99] op_sel_hi:[1,0,0]
	v_exp_f32_e32 v67, v67
	v_exp_f32_e32 v68, v68
	v_pk_fma_f32 v[66:67], v[66:67], s[98:99], s[98:99] op_sel_hi:[1,0,0]
	v_exp_f32_e32 v69, v69
	v_exp_f32_e32 v70, v70
	v_pk_add_f32 v[68:69], v[68:69], 1.0 op_sel_hi:[1,0]
	v_exp_f32_e32 v71, v71
	v_pk_mul_f32 v[64:65], v[64:65], v[68:69]
	v_rcp_f32_e32 v64, v64
	v_pk_add_f32 v[70:71], v[70:71], 1.0 op_sel_hi:[1,0]
	v_rcp_f32_e32 v65, v65
	v_pk_mul_f32 v[66:67], v[66:67], v[70:71]
	v_pk_add_f32 v[68:69], v[68:69], 2.0 op_sel_hi:[1,0] neg_lo:[1,0] neg_hi:[1,0]
	v_rcp_f32_e32 v66, v66
	v_rcp_f32_e32 v67, v67
	v_pk_add_f32 v[70:71], v[70:71], 2.0 op_sel_hi:[1,0] neg_lo:[1,0] neg_hi:[1,0]
	v_pk_mul_f32 v[64:65], v[64:65], v[68:69]
	v_pk_mul_f32 v[66:67], v[66:67], v[70:71]
	v_ashrrev_i32_e32 v203, 31, v202
	v_cvt_pk_fp8_f32 v72, v64, v65
	s_and_b64 vcc, exec, s[0:1]
	v_cvt_pk_fp8_f32 v72, v66, v67 op_sel:[0,0,1]
	v_lshlrev_b64 v[68:69], 10, v[202:203]
	v_lshl_add_u64 v[70:71], v[122:123], 0, v[68:69]
	global_store_dword v[70:71], v72, off
	v_exp_f32_e32 v56, v56
	v_exp_f32_e32 v57, v57
	v_exp_f32_e32 v58, v58
	v_pk_add_f32 v[56:57], v[56:57], 1.0 op_sel_hi:[1,0]
	v_exp_f32_e32 v59, v59
	v_exp_f32_e32 v60, v60
	v_pk_add_f32 v[58:59], v[58:59], 1.0 op_sel_hi:[1,0]
	v_exp_f32_e32 v61, v61
	v_exp_f32_e32 v62, v62
	v_pk_add_f32 v[60:61], v[60:61], 1.0 op_sel_hi:[1,0]
	v_exp_f32_e32 v63, v63
	v_exp_f32_e32 v52, v52
	v_pk_add_f32 v[62:63], v[62:63], 1.0 op_sel_hi:[1,0]
	v_exp_f32_e32 v53, v53
	v_pk_mul_f32 v[56:57], v[56:57], v[60:61]
	v_exp_f32_e32 v54, v54
	v_pk_mul_f32 v[58:59], v[58:59], v[62:63]
	v_exp_f32_e32 v55, v55
	v_pk_add_f32 v[60:61], v[60:61], 2.0 op_sel_hi:[1,0] neg_lo:[1,0] neg_hi:[1,0]
	v_pk_add_f32 v[52:53], v[52:53], 1.0 op_sel_hi:[1,0]
	v_pk_add_f32 v[62:63], v[62:63], 2.0 op_sel_hi:[1,0] neg_lo:[1,0] neg_hi:[1,0]
	v_pk_add_f32 v[54:55], v[54:55], 1.0 op_sel_hi:[1,0]
	v_pk_mul_f32 v[60:61], v[60:61], v[52:53]
	v_pk_mul_f32 v[52:53], v[52:53], v[56:57]
	v_pk_mul_f32 v[62:63], v[62:63], v[54:55]
	v_pk_mul_f32 v[54:55], v[54:55], v[58:59]
	v_rcp_f32_e32 v52, v52
	v_rcp_f32_e32 v53, v53
	v_rcp_f32_e32 v54, v54
	v_rcp_f32_e32 v55, v55
	s_waitcnt vmcnt(8)
	v_pk_fma_f32 v[60:61], v[156:157], v[56:57], v[60:61]
	v_pk_fma_f32 v[62:63], v[158:159], v[58:59], v[62:63]
	v_pk_mul_f32 v[52:53], v[52:53], v[60:61]
	v_pk_mul_f32 v[54:55], v[54:55], v[62:63]
	v_lshl_add_u64 v[56:57], v[176:177], 0, s[14:15]
	global_store_dwordx4 v[56:57], v[52:55], off nt
	s_nop 1
	v_pk_mul_f32 v[52:53], v[52:53], s[96:97] op_sel_hi:[1,0]
	v_pk_mul_f32 v[54:55], v[54:55], s[96:97] op_sel_hi:[1,0]
	v_exp_f32_e32 v48, v48
	v_exp_f32_e32 v49, v49
	v_exp_f32_e32 v50, v50
	v_pk_fma_f32 v[48:49], v[48:49], s[98:99], s[98:99] op_sel_hi:[1,0,0]
	v_exp_f32_e32 v51, v51
	v_exp_f32_e32 v52, v52
	v_pk_fma_f32 v[50:51], v[50:51], s[98:99], s[98:99] op_sel_hi:[1,0,0]
	v_exp_f32_e32 v53, v53
	v_exp_f32_e32 v54, v54
	v_pk_add_f32 v[52:53], v[52:53], 1.0 op_sel_hi:[1,0]
	v_exp_f32_e32 v55, v55
	v_pk_mul_f32 v[48:49], v[48:49], v[52:53]
	v_rcp_f32_e32 v48, v48
	v_pk_add_f32 v[54:55], v[54:55], 1.0 op_sel_hi:[1,0]
	v_rcp_f32_e32 v49, v49
	v_pk_mul_f32 v[50:51], v[50:51], v[54:55]
	v_pk_add_f32 v[52:53], v[52:53], 2.0 op_sel_hi:[1,0] neg_lo:[1,0] neg_hi:[1,0]
	v_rcp_f32_e32 v50, v50
	v_rcp_f32_e32 v51, v51
	v_pk_add_f32 v[54:55], v[54:55], 2.0 op_sel_hi:[1,0] neg_lo:[1,0] neg_hi:[1,0]
	v_pk_mul_f32 v[48:49], v[48:49], v[52:53]
	v_pk_mul_f32 v[50:51], v[50:51], v[54:55]
	v_ashrrev_i32_e32 v201, 31, v200
	v_cvt_pk_fp8_f32 v56, v48, v49
	s_and_b64 vcc, exec, s[0:1]
	v_cvt_pk_fp8_f32 v56, v50, v51 op_sel:[0,0,1]
	v_lshlrev_b64 v[52:53], 10, v[200:201]
	v_lshl_add_u64 v[54:55], v[122:123], 0, v[52:53]
	global_store_dword v[54:55], v56, off
	v_exp_f32_e32 v40, v40
	v_exp_f32_e32 v41, v41
	v_exp_f32_e32 v42, v42
	v_pk_add_f32 v[40:41], v[40:41], 1.0 op_sel_hi:[1,0]
	v_exp_f32_e32 v43, v43
	v_exp_f32_e32 v44, v44
	v_pk_add_f32 v[42:43], v[42:43], 1.0 op_sel_hi:[1,0]
	v_exp_f32_e32 v45, v45
	v_exp_f32_e32 v46, v46
	v_pk_add_f32 v[44:45], v[44:45], 1.0 op_sel_hi:[1,0]
	v_exp_f32_e32 v47, v47
	v_exp_f32_e32 v36, v36
	v_pk_add_f32 v[46:47], v[46:47], 1.0 op_sel_hi:[1,0]
	v_exp_f32_e32 v37, v37
	v_pk_mul_f32 v[40:41], v[40:41], v[44:45]
	v_exp_f32_e32 v38, v38
	v_pk_mul_f32 v[42:43], v[42:43], v[46:47]
	v_exp_f32_e32 v39, v39
	v_pk_add_f32 v[44:45], v[44:45], 2.0 op_sel_hi:[1,0] neg_lo:[1,0] neg_hi:[1,0]
	v_pk_add_f32 v[36:37], v[36:37], 1.0 op_sel_hi:[1,0]
	v_pk_add_f32 v[46:47], v[46:47], 2.0 op_sel_hi:[1,0] neg_lo:[1,0] neg_hi:[1,0]
	v_pk_add_f32 v[38:39], v[38:39], 1.0 op_sel_hi:[1,0]
	v_pk_mul_f32 v[44:45], v[44:45], v[36:37]
	v_pk_mul_f32 v[36:37], v[36:37], v[40:41]
	v_pk_mul_f32 v[46:47], v[46:47], v[38:39]
	v_pk_mul_f32 v[38:39], v[38:39], v[42:43]
	v_rcp_f32_e32 v36, v36
	v_rcp_f32_e32 v37, v37
	v_rcp_f32_e32 v38, v38
	v_rcp_f32_e32 v39, v39
	v_pk_fma_f32 v[44:45], v[152:153], v[40:41], v[44:45]
	v_pk_fma_f32 v[46:47], v[154:155], v[42:43], v[46:47]
	v_lshl_add_u64 v[40:41], v[176:177], 0, s[22:23]
	v_pk_mul_f32 v[36:37], v[36:37], v[44:45]
	v_pk_mul_f32 v[38:39], v[38:39], v[46:47]
	global_store_dwordx4 v[40:41], v[36:39], off nt
	s_nop 1
	v_pk_mul_f32 v[36:37], v[36:37], s[96:97] op_sel_hi:[1,0]
	v_pk_mul_f32 v[38:39], v[38:39], s[96:97] op_sel_hi:[1,0]
	v_exp_f32_e32 v32, v32
	v_exp_f32_e32 v33, v33
	v_exp_f32_e32 v34, v34
	v_pk_fma_f32 v[32:33], v[32:33], s[98:99], s[98:99] op_sel_hi:[1,0,0]
	v_exp_f32_e32 v35, v35
	v_exp_f32_e32 v36, v36
	v_pk_fma_f32 v[34:35], v[34:35], s[98:99], s[98:99] op_sel_hi:[1,0,0]
	v_exp_f32_e32 v37, v37
	v_exp_f32_e32 v38, v38
	v_pk_add_f32 v[36:37], v[36:37], 1.0 op_sel_hi:[1,0]
	v_exp_f32_e32 v39, v39
	v_pk_mul_f32 v[32:33], v[32:33], v[36:37]
	v_rcp_f32_e32 v32, v32
	v_pk_add_f32 v[38:39], v[38:39], 1.0 op_sel_hi:[1,0]
	v_rcp_f32_e32 v33, v33
	v_pk_mul_f32 v[34:35], v[34:35], v[38:39]
	v_pk_add_f32 v[36:37], v[36:37], 2.0 op_sel_hi:[1,0] neg_lo:[1,0] neg_hi:[1,0]
	v_rcp_f32_e32 v34, v34
	v_rcp_f32_e32 v35, v35
	v_pk_add_f32 v[38:39], v[38:39], 2.0 op_sel_hi:[1,0] neg_lo:[1,0] neg_hi:[1,0]
	v_pk_mul_f32 v[32:33], v[32:33], v[36:37]
	v_pk_mul_f32 v[34:35], v[34:35], v[38:39]
	v_cvt_pk_fp8_f32 v40, v32, v33
	v_or_b32_e32 v36, 16, v200
	v_ashrrev_i32_e32 v37, 31, v36
	v_lshlrev_b64 v[36:37], 10, v[36:37]
	v_cvt_pk_fp8_f32 v40, v34, v35 op_sel:[0,0,1]
	v_lshl_add_u64 v[38:39], v[122:123], 0, v[36:37]
	global_store_dword v[38:39], v40, off
	v_exp_f32_e32 v24, v24
	v_exp_f32_e32 v25, v25
	v_exp_f32_e32 v26, v26
	v_pk_add_f32 v[24:25], v[24:25], 1.0 op_sel_hi:[1,0]
	v_exp_f32_e32 v27, v27
	v_exp_f32_e32 v28, v28
	v_pk_add_f32 v[26:27], v[26:27], 1.0 op_sel_hi:[1,0]
	v_exp_f32_e32 v29, v29
	v_exp_f32_e32 v30, v30
	v_pk_add_f32 v[28:29], v[28:29], 1.0 op_sel_hi:[1,0]
	v_exp_f32_e32 v31, v31
	v_exp_f32_e32 v20, v20
	v_pk_add_f32 v[30:31], v[30:31], 1.0 op_sel_hi:[1,0]
	v_exp_f32_e32 v21, v21
	v_pk_mul_f32 v[24:25], v[24:25], v[28:29]
	v_exp_f32_e32 v22, v22
	v_pk_mul_f32 v[26:27], v[26:27], v[30:31]
	v_exp_f32_e32 v23, v23
	v_pk_add_f32 v[28:29], v[28:29], 2.0 op_sel_hi:[1,0] neg_lo:[1,0] neg_hi:[1,0]
	v_pk_add_f32 v[20:21], v[20:21], 1.0 op_sel_hi:[1,0]
	v_pk_add_f32 v[30:31], v[30:31], 2.0 op_sel_hi:[1,0] neg_lo:[1,0] neg_hi:[1,0]
	v_pk_add_f32 v[22:23], v[22:23], 1.0 op_sel_hi:[1,0]
	v_pk_mul_f32 v[28:29], v[28:29], v[20:21]
	v_pk_mul_f32 v[20:21], v[20:21], v[24:25]
	v_pk_mul_f32 v[30:31], v[30:31], v[22:23]
	v_pk_mul_f32 v[22:23], v[22:23], v[26:27]
	v_rcp_f32_e32 v20, v20
	v_rcp_f32_e32 v21, v21
	v_rcp_f32_e32 v22, v22
	v_rcp_f32_e32 v23, v23
	v_pk_fma_f32 v[28:29], v[148:149], v[24:25], v[28:29]
	v_pk_fma_f32 v[30:31], v[150:151], v[26:27], v[30:31]
	v_pk_mul_f32 v[20:21], v[20:21], v[28:29]
	v_pk_mul_f32 v[22:23], v[22:23], v[30:31]
	v_lshl_add_u64 v[24:25], v[176:177], 0, s[16:17]
	global_store_dwordx4 v[24:25], v[20:23], off nt
	s_nop 1
	v_pk_mul_f32 v[20:21], v[20:21], s[96:97] op_sel_hi:[1,0]
	v_pk_mul_f32 v[22:23], v[22:23], s[96:97] op_sel_hi:[1,0]
	v_exp_f32_e32 v16, v16
	v_exp_f32_e32 v17, v17
	v_exp_f32_e32 v18, v18
	v_pk_fma_f32 v[16:17], v[16:17], s[98:99], s[98:99] op_sel_hi:[1,0,0]
	v_exp_f32_e32 v19, v19
	v_exp_f32_e32 v20, v20
	v_pk_fma_f32 v[18:19], v[18:19], s[98:99], s[98:99] op_sel_hi:[1,0,0]
	v_exp_f32_e32 v21, v21
	v_exp_f32_e32 v22, v22
	v_pk_add_f32 v[20:21], v[20:21], 1.0 op_sel_hi:[1,0]
	v_exp_f32_e32 v23, v23
	v_pk_mul_f32 v[16:17], v[16:17], v[20:21]
	v_rcp_f32_e32 v16, v16
	v_pk_add_f32 v[22:23], v[22:23], 1.0 op_sel_hi:[1,0]
	v_rcp_f32_e32 v17, v17
	v_pk_mul_f32 v[18:19], v[18:19], v[22:23]
	v_pk_add_f32 v[20:21], v[20:21], 2.0 op_sel_hi:[1,0] neg_lo:[1,0] neg_hi:[1,0]
	v_rcp_f32_e32 v18, v18
	v_rcp_f32_e32 v19, v19
	v_pk_add_f32 v[22:23], v[22:23], 2.0 op_sel_hi:[1,0] neg_lo:[1,0] neg_hi:[1,0]
	v_pk_mul_f32 v[16:17], v[16:17], v[20:21]
	v_pk_mul_f32 v[18:19], v[18:19], v[22:23]
	v_cvt_pk_fp8_f32 v24, v16, v17
	v_or_b32_e32 v20, 32, v200
	v_ashrrev_i32_e32 v21, 31, v20
	v_lshlrev_b64 v[20:21], 10, v[20:21]
	v_cvt_pk_fp8_f32 v24, v18, v19 op_sel:[0,0,1]
	v_lshl_add_u64 v[22:23], v[122:123], 0, v[20:21]
	global_store_dword v[22:23], v24, off
	v_exp_f32_e32 v8, v8
	v_exp_f32_e32 v9, v9
	v_exp_f32_e32 v10, v10
	v_pk_add_f32 v[8:9], v[8:9], 1.0 op_sel_hi:[1,0]
	v_exp_f32_e32 v11, v11
	v_exp_f32_e32 v12, v12
	v_pk_add_f32 v[10:11], v[10:11], 1.0 op_sel_hi:[1,0]
	v_exp_f32_e32 v13, v13
	v_exp_f32_e32 v14, v14
	v_pk_add_f32 v[12:13], v[12:13], 1.0 op_sel_hi:[1,0]
	v_exp_f32_e32 v15, v15
	v_exp_f32_e32 v4, v4
	v_pk_add_f32 v[14:15], v[14:15], 1.0 op_sel_hi:[1,0]
	v_exp_f32_e32 v5, v5
	v_pk_mul_f32 v[8:9], v[8:9], v[12:13]
	v_exp_f32_e32 v6, v6
	v_pk_mul_f32 v[10:11], v[10:11], v[14:15]
	v_exp_f32_e32 v7, v7
	v_pk_add_f32 v[12:13], v[12:13], 2.0 op_sel_hi:[1,0] neg_lo:[1,0] neg_hi:[1,0]
	v_pk_add_f32 v[4:5], v[4:5], 1.0 op_sel_hi:[1,0]
	v_pk_add_f32 v[14:15], v[14:15], 2.0 op_sel_hi:[1,0] neg_lo:[1,0] neg_hi:[1,0]
	v_pk_add_f32 v[6:7], v[6:7], 1.0 op_sel_hi:[1,0]
	v_pk_mul_f32 v[12:13], v[12:13], v[4:5]
	v_pk_mul_f32 v[4:5], v[4:5], v[8:9]
	v_pk_mul_f32 v[14:15], v[14:15], v[6:7]
	v_pk_mul_f32 v[6:7], v[6:7], v[10:11]
	v_rcp_f32_e32 v4, v4
	v_rcp_f32_e32 v5, v5
	v_rcp_f32_e32 v6, v6
	v_rcp_f32_e32 v7, v7
	v_pk_fma_f32 v[12:13], v[144:145], v[8:9], v[12:13]
	v_pk_fma_f32 v[14:15], v[146:147], v[10:11], v[14:15]
	v_lshl_add_u64 v[8:9], v[176:177], 0, s[24:25]
	v_pk_mul_f32 v[4:5], v[4:5], v[12:13]
	v_pk_mul_f32 v[6:7], v[6:7], v[14:15]
	global_store_dwordx4 v[8:9], v[4:7], off nt
	s_nop 1
	v_pk_mul_f32 v[4:5], v[4:5], s[96:97] op_sel_hi:[1,0]
	v_pk_mul_f32 v[6:7], v[6:7], s[96:97] op_sel_hi:[1,0]
	v_exp_f32_e32 v0, v0
	v_exp_f32_e32 v1, v1
	v_exp_f32_e32 v2, v2
	v_pk_fma_f32 v[0:1], v[0:1], s[98:99], s[98:99] op_sel_hi:[1,0,0]
	v_exp_f32_e32 v3, v3
	v_exp_f32_e32 v4, v4
	v_pk_fma_f32 v[2:3], v[2:3], s[98:99], s[98:99] op_sel_hi:[1,0,0]
	v_exp_f32_e32 v5, v5
	v_exp_f32_e32 v6, v6
	v_pk_add_f32 v[4:5], v[4:5], 1.0 op_sel_hi:[1,0]
	v_exp_f32_e32 v7, v7
	v_pk_mul_f32 v[0:1], v[0:1], v[4:5]
	v_rcp_f32_e32 v0, v0
	v_pk_add_f32 v[6:7], v[6:7], 1.0 op_sel_hi:[1,0]
	v_rcp_f32_e32 v1, v1
	v_pk_mul_f32 v[2:3], v[2:3], v[6:7]
	v_pk_add_f32 v[4:5], v[4:5], 2.0 op_sel_hi:[1,0] neg_lo:[1,0] neg_hi:[1,0]
	v_rcp_f32_e32 v2, v2
	v_rcp_f32_e32 v3, v3
	v_pk_add_f32 v[6:7], v[6:7], 2.0 op_sel_hi:[1,0] neg_lo:[1,0] neg_hi:[1,0]
	v_pk_mul_f32 v[0:1], v[0:1], v[4:5]
	v_pk_mul_f32 v[2:3], v[2:3], v[6:7]
	v_cvt_pk_fp8_f32 v8, v0, v1
	v_or_b32_e32 v4, 48, v200
	v_ashrrev_i32_e32 v5, 31, v4
	v_lshlrev_b64 v[4:5], 10, v[4:5]
	v_cvt_pk_fp8_f32 v8, v2, v3 op_sel:[0,0,1]
	v_lshl_add_u64 v[6:7], v[122:123], 0, v[4:5]
	global_store_dword v[6:7], v8, off
	s_branch .LBB2_24
.Lmy_epi_nl7:
	v_exp_f32_e32 v120, v120
	v_exp_f32_e32 v121, v121
	v_exp_f32_e32 v122, v122
	v_pk_add_f32 v[120:121], v[120:121], 1.0 op_sel_hi:[1,0]
	v_exp_f32_e32 v123, v123
	v_exp_f32_e32 v124, v124
	v_pk_add_f32 v[122:123], v[122:123], 1.0 op_sel_hi:[1,0]
	v_exp_f32_e32 v125, v125
	v_exp_f32_e32 v126, v126
	v_pk_add_f32 v[124:125], v[124:125], 1.0 op_sel_hi:[1,0]
	v_exp_f32_e32 v127, v127
	v_exp_f32_e32 v116, v116
	v_pk_add_f32 v[126:127], v[126:127], 1.0 op_sel_hi:[1,0]
	v_exp_f32_e32 v117, v117
	v_pk_mul_f32 v[120:121], v[120:121], v[124:125]
	v_exp_f32_e32 v118, v118
	v_pk_mul_f32 v[122:123], v[122:123], v[126:127]
	v_exp_f32_e32 v119, v119
	v_pk_add_f32 v[124:125], v[124:125], 2.0 op_sel_hi:[1,0] neg_lo:[1,0] neg_hi:[1,0]
	v_pk_add_f32 v[116:117], v[116:117], 1.0 op_sel_hi:[1,0]
	v_pk_add_f32 v[126:127], v[126:127], 2.0 op_sel_hi:[1,0] neg_lo:[1,0] neg_hi:[1,0]
	v_pk_add_f32 v[118:119], v[118:119], 1.0 op_sel_hi:[1,0]
	v_pk_mul_f32 v[124:125], v[124:125], v[116:117]
	v_pk_mul_f32 v[116:117], v[116:117], v[120:121]
	v_pk_mul_f32 v[126:127], v[126:127], v[118:119]
	v_pk_mul_f32 v[118:119], v[118:119], v[122:123]
	v_rcp_f32_e32 v116, v116
	v_rcp_f32_e32 v117, v117
	v_rcp_f32_e32 v118, v118
	v_rcp_f32_e32 v119, v119
	s_waitcnt lgkmcnt(3)
	v_pk_fma_f32 v[124:125], v[172:173], v[120:121], v[124:125]
	v_pk_fma_f32 v[126:127], v[174:175], v[122:123], v[126:127]
	v_pk_mul_f32 v[116:117], v[116:117], v[124:125]
	v_pk_mul_f32 v[118:119], v[118:119], v[126:127]
	global_store_dwordx4 v[176:177], v[116:119], off nt
	s_nop 1
	v_pk_mul_f32 v[116:117], v[116:117], s[96:97] op_sel_hi:[1,0]
	v_pk_mul_f32 v[118:119], v[118:119], s[96:97] op_sel_hi:[1,0]
	v_exp_f32_e32 v112, v112
	v_exp_f32_e32 v113, v113
	v_exp_f32_e32 v114, v114
	v_pk_fma_f32 v[112:113], v[112:113], s[98:99], s[98:99] op_sel_hi:[1,0,0]
	v_exp_f32_e32 v115, v115
	v_exp_f32_e32 v116, v116
	v_pk_fma_f32 v[114:115], v[114:115], s[98:99], s[98:99] op_sel_hi:[1,0,0]
	v_exp_f32_e32 v117, v117
	v_exp_f32_e32 v118, v118
	v_pk_add_f32 v[116:117], v[116:117], 1.0 op_sel_hi:[1,0]
	v_exp_f32_e32 v119, v119
	v_pk_mul_f32 v[112:113], v[112:113], v[116:117]
	v_rcp_f32_e32 v112, v112
	v_pk_add_f32 v[118:119], v[118:119], 1.0 op_sel_hi:[1,0]
	v_rcp_f32_e32 v113, v113
	v_pk_mul_f32 v[114:115], v[114:115], v[118:119]
	v_pk_add_f32 v[116:117], v[116:117], 2.0 op_sel_hi:[1,0] neg_lo:[1,0] neg_hi:[1,0]
	v_rcp_f32_e32 v114, v114
	v_rcp_f32_e32 v115, v115
	v_pk_add_f32 v[118:119], v[118:119], 2.0 op_sel_hi:[1,0] neg_lo:[1,0] neg_hi:[1,0]
	v_pk_mul_f32 v[112:113], v[112:113], v[116:117]
	v_pk_mul_f32 v[114:115], v[114:115], v[118:119]
	v_cvt_pk_fp8_f32 v124, v112, v113
	s_add_u32 s0, s8, s27
	s_addc_u32 s1, s9, 0
	s_ashr_i32 s35, s34, 31
	s_lshl_b64 s[34:35], s[34:35], 21
	v_ashrrev_i32_e32 v209, 31, v208
	s_add_u32 s36, s73, s34
	v_lshrrev_b32_e32 v126, 4, v210
	v_and_b32_e32 v127, 15, v210
	v_lshl_or_b32 v126, v126, 8, v127
	v_and_b32_e32 v127, 15, v208
	v_mul_u32_u24_e32 v127, 0x3f0, v127
	v_sub_u32_e32 v126, v126, v127
	v_ashrrev_i32_e32 v127, 31, v126
	v_lshl_add_u64 v[122:123], s[0:1], 0, v[126:127]
	v_cvt_pk_fp8_f32 v124, v114, v115 op_sel:[0,0,1]
	v_lshlrev_b64 v[116:117], 10, v[208:209]
	s_addc_u32 s37, s74, s35
	v_lshl_add_u64 v[118:119], v[122:123], 0, v[116:117]
	global_store_dword v[118:119], v124, off
	s_cmp_eq_u32 s30, 7
	s_cselect_b64 s[34:35], -1, 0
	s_cmp_lg_u32 s30, 7
	v_lshrrev_b32_e32 v126, 4, v210
	v_lshlrev_b32_e32 v126, 9, v126
	v_and_b32_e32 v127, 15, v210
	v_lshl_or_b32 v126, v127, 1, v126
	v_and_b32_e32 v127, 15, v208
	v_mul_u32_u24_e32 v127, 0x7e0, v127
	v_sub_u32_e32 v126, v126, v127
	v_ashrrev_i32_e32 v127, 31, v126
	v_lshl_add_u64 v[120:121], s[36:37], 0, v[126:127]
	v_pk_mul_f32 v[112:113], v[112:113], s[98:99] op_sel_hi:[1,0]
	v_pk_mul_f32 v[114:115], v[114:115], s[98:99] op_sel_hi:[1,0]
	v_cvt_pk_f16_f32 v112, v112, v113
	v_cvt_pk_f16_f32 v113, v114, v115
	v_lshl_add_u64 v[114:115], v[116:117], 1, v[120:121]
	global_store_dwordx2 v[114:115], v[112:113], off
	v_exp_f32_e32 v104, v104
	v_exp_f32_e32 v105, v105
	v_exp_f32_e32 v106, v106
	v_pk_add_f32 v[104:105], v[104:105], 1.0 op_sel_hi:[1,0]
	v_exp_f32_e32 v107, v107
	v_exp_f32_e32 v108, v108
	v_pk_add_f32 v[106:107], v[106:107], 1.0 op_sel_hi:[1,0]
	v_exp_f32_e32 v109, v109
	v_exp_f32_e32 v110, v110
	v_pk_add_f32 v[108:109], v[108:109], 1.0 op_sel_hi:[1,0]
	v_exp_f32_e32 v111, v111
	v_exp_f32_e32 v100, v100
	v_pk_add_f32 v[110:111], v[110:111], 1.0 op_sel_hi:[1,0]
	v_exp_f32_e32 v101, v101
	v_pk_mul_f32 v[104:105], v[104:105], v[108:109]
	v_exp_f32_e32 v102, v102
	v_pk_mul_f32 v[106:107], v[106:107], v[110:111]
	v_exp_f32_e32 v103, v103
	v_pk_add_f32 v[108:109], v[108:109], 2.0 op_sel_hi:[1,0] neg_lo:[1,0] neg_hi:[1,0]
	v_pk_add_f32 v[100:101], v[100:101], 1.0 op_sel_hi:[1,0]
	v_pk_add_f32 v[110:111], v[110:111], 2.0 op_sel_hi:[1,0] neg_lo:[1,0] neg_hi:[1,0]
	v_pk_add_f32 v[102:103], v[102:103], 1.0 op_sel_hi:[1,0]
	v_pk_mul_f32 v[108:109], v[108:109], v[100:101]
	v_pk_mul_f32 v[100:101], v[100:101], v[104:105]
	v_pk_mul_f32 v[110:111], v[110:111], v[102:103]
	v_pk_mul_f32 v[102:103], v[102:103], v[106:107]
	v_rcp_f32_e32 v100, v100
	v_rcp_f32_e32 v101, v101
	v_rcp_f32_e32 v102, v102
	v_rcp_f32_e32 v103, v103
	s_waitcnt lgkmcnt(2)
	v_pk_fma_f32 v[108:109], v[168:169], v[104:105], v[108:109]
	v_pk_fma_f32 v[110:111], v[170:171], v[106:107], v[110:111]
	v_lshl_add_u64 v[104:105], v[176:177], 0, s[18:19]
	v_pk_mul_f32 v[100:101], v[100:101], v[108:109]
	v_pk_mul_f32 v[102:103], v[102:103], v[110:111]
	global_store_dwordx4 v[104:105], v[100:103], off nt
	s_nop 1
	v_pk_mul_f32 v[100:101], v[100:101], s[96:97] op_sel_hi:[1,0]
	v_pk_mul_f32 v[102:103], v[102:103], s[96:97] op_sel_hi:[1,0]
	v_exp_f32_e32 v96, v96
	v_exp_f32_e32 v97, v97
	v_exp_f32_e32 v98, v98
	v_pk_fma_f32 v[96:97], v[96:97], s[98:99], s[98:99] op_sel_hi:[1,0,0]
	v_exp_f32_e32 v99, v99
	v_exp_f32_e32 v100, v100
	v_pk_fma_f32 v[98:99], v[98:99], s[98:99], s[98:99] op_sel_hi:[1,0,0]
	v_exp_f32_e32 v101, v101
	v_exp_f32_e32 v102, v102
	v_pk_add_f32 v[100:101], v[100:101], 1.0 op_sel_hi:[1,0]
	v_exp_f32_e32 v103, v103
	v_pk_mul_f32 v[96:97], v[96:97], v[100:101]
	v_rcp_f32_e32 v96, v96
	v_pk_add_f32 v[102:103], v[102:103], 1.0 op_sel_hi:[1,0]
	v_rcp_f32_e32 v97, v97
	v_pk_mul_f32 v[98:99], v[98:99], v[102:103]
	v_pk_add_f32 v[100:101], v[100:101], 2.0 op_sel_hi:[1,0] neg_lo:[1,0] neg_hi:[1,0]
	v_rcp_f32_e32 v98, v98
	v_rcp_f32_e32 v99, v99
	v_pk_add_f32 v[102:103], v[102:103], 2.0 op_sel_hi:[1,0] neg_lo:[1,0] neg_hi:[1,0]
	v_pk_mul_f32 v[96:97], v[96:97], v[100:101]
	v_pk_mul_f32 v[98:99], v[98:99], v[102:103]
	v_cvt_pk_fp8_f32 v104, v96, v97
	v_ashrrev_i32_e32 v207, 31, v206
	v_lshlrev_b64 v[100:101], 10, v[206:207]
	v_lshl_add_u64 v[102:103], v[122:123], 0, v[100:101]
	v_cvt_pk_fp8_f32 v104, v98, v99 op_sel:[0,0,1]
	v_cndmask_b32_e64 v105, 0, 1, s[34:35]
	global_store_dword v[102:103], v104, off
	v_cmp_ne_u32_e64 s[0:1], 1, v105
	v_pk_mul_f32 v[96:97], v[96:97], s[98:99] op_sel_hi:[1,0]
	v_pk_mul_f32 v[98:99], v[98:99], s[98:99] op_sel_hi:[1,0]
	v_cvt_pk_f16_f32 v96, v96, v97
	v_cvt_pk_f16_f32 v97, v98, v99
	v_lshl_add_u64 v[98:99], v[100:101], 1, v[120:121]
	global_store_dwordx2 v[98:99], v[96:97], off
	v_exp_f32_e32 v88, v88
	v_exp_f32_e32 v89, v89
	v_exp_f32_e32 v90, v90
	v_pk_add_f32 v[88:89], v[88:89], 1.0 op_sel_hi:[1,0]
	v_exp_f32_e32 v91, v91
	v_exp_f32_e32 v92, v92
	v_pk_add_f32 v[90:91], v[90:91], 1.0 op_sel_hi:[1,0]
	v_exp_f32_e32 v93, v93
	v_exp_f32_e32 v94, v94
	v_pk_add_f32 v[92:93], v[92:93], 1.0 op_sel_hi:[1,0]
	v_exp_f32_e32 v95, v95
	v_exp_f32_e32 v84, v84
	v_pk_add_f32 v[94:95], v[94:95], 1.0 op_sel_hi:[1,0]
	v_exp_f32_e32 v85, v85
	v_pk_mul_f32 v[88:89], v[88:89], v[92:93]
	v_exp_f32_e32 v86, v86
	v_pk_mul_f32 v[90:91], v[90:91], v[94:95]
	v_exp_f32_e32 v87, v87
	v_pk_add_f32 v[92:93], v[92:93], 2.0 op_sel_hi:[1,0] neg_lo:[1,0] neg_hi:[1,0]
	v_pk_add_f32 v[84:85], v[84:85], 1.0 op_sel_hi:[1,0]
	v_pk_add_f32 v[94:95], v[94:95], 2.0 op_sel_hi:[1,0] neg_lo:[1,0] neg_hi:[1,0]
	v_pk_add_f32 v[86:87], v[86:87], 1.0 op_sel_hi:[1,0]
	v_pk_mul_f32 v[92:93], v[92:93], v[84:85]
	v_pk_mul_f32 v[84:85], v[84:85], v[88:89]
	v_pk_mul_f32 v[94:95], v[94:95], v[86:87]
	v_pk_mul_f32 v[86:87], v[86:87], v[90:91]
	v_rcp_f32_e32 v84, v84
	v_rcp_f32_e32 v85, v85
	v_rcp_f32_e32 v86, v86
	v_rcp_f32_e32 v87, v87
	s_waitcnt lgkmcnt(1)
	v_pk_fma_f32 v[92:93], v[164:165], v[88:89], v[92:93]
	v_pk_fma_f32 v[94:95], v[166:167], v[90:91], v[94:95]
	v_pk_mul_f32 v[84:85], v[84:85], v[92:93]
	v_pk_mul_f32 v[86:87], v[86:87], v[94:95]
	v_lshl_add_u64 v[88:89], v[176:177], 0, s[12:13]
	global_store_dwordx4 v[88:89], v[84:87], off nt
	s_nop 1
	v_pk_mul_f32 v[84:85], v[84:85], s[96:97] op_sel_hi:[1,0]
	v_pk_mul_f32 v[86:87], v[86:87], s[96:97] op_sel_hi:[1,0]
	v_exp_f32_e32 v80, v80
	v_exp_f32_e32 v81, v81
	v_exp_f32_e32 v82, v82
	v_pk_fma_f32 v[80:81], v[80:81], s[98:99], s[98:99] op_sel_hi:[1,0,0]
	v_exp_f32_e32 v83, v83
	v_exp_f32_e32 v84, v84
	v_pk_fma_f32 v[82:83], v[82:83], s[98:99], s[98:99] op_sel_hi:[1,0,0]
	v_exp_f32_e32 v85, v85
	v_exp_f32_e32 v86, v86
	v_pk_add_f32 v[84:85], v[84:85], 1.0 op_sel_hi:[1,0]
	v_exp_f32_e32 v87, v87
	v_pk_mul_f32 v[80:81], v[80:81], v[84:85]
	v_rcp_f32_e32 v80, v80
	v_pk_add_f32 v[86:87], v[86:87], 1.0 op_sel_hi:[1,0]
	v_rcp_f32_e32 v81, v81
	v_pk_mul_f32 v[82:83], v[82:83], v[86:87]
	v_pk_add_f32 v[84:85], v[84:85], 2.0 op_sel_hi:[1,0] neg_lo:[1,0] neg_hi:[1,0]
	v_rcp_f32_e32 v82, v82
	v_rcp_f32_e32 v83, v83
	v_pk_add_f32 v[86:87], v[86:87], 2.0 op_sel_hi:[1,0] neg_lo:[1,0] neg_hi:[1,0]
	v_pk_mul_f32 v[80:81], v[80:81], v[84:85]
	v_pk_mul_f32 v[82:83], v[82:83], v[86:87]
	v_ashrrev_i32_e32 v205, 31, v204
	v_cvt_pk_fp8_f32 v88, v80, v81
	s_and_b64 vcc, exec, s[0:1]
	v_cvt_pk_fp8_f32 v88, v82, v83 op_sel:[0,0,1]
	v_lshlrev_b64 v[84:85], 10, v[204:205]
	v_lshl_add_u64 v[86:87], v[122:123], 0, v[84:85]
	global_store_dword v[86:87], v88, off
	v_pk_mul_f32 v[80:81], v[80:81], s[98:99] op_sel_hi:[1,0]
	v_pk_mul_f32 v[82:83], v[82:83], s[98:99] op_sel_hi:[1,0]
	v_cvt_pk_f16_f32 v80, v80, v81
	v_cvt_pk_f16_f32 v81, v82, v83
	v_lshl_add_u64 v[82:83], v[84:85], 1, v[120:121]
	global_store_dwordx2 v[82:83], v[80:81], off
	v_exp_f32_e32 v72, v72
	v_exp_f32_e32 v73, v73
	v_exp_f32_e32 v74, v74
	v_pk_add_f32 v[72:73], v[72:73], 1.0 op_sel_hi:[1,0]
	v_exp_f32_e32 v75, v75
	v_exp_f32_e32 v76, v76
	v_pk_add_f32 v[74:75], v[74:75], 1.0 op_sel_hi:[1,0]
	v_exp_f32_e32 v77, v77
	v_exp_f32_e32 v78, v78
	v_pk_add_f32 v[76:77], v[76:77], 1.0 op_sel_hi:[1,0]
	v_exp_f32_e32 v79, v79
	v_exp_f32_e32 v68, v68
	v_pk_add_f32 v[78:79], v[78:79], 1.0 op_sel_hi:[1,0]
	v_exp_f32_e32 v69, v69
	v_pk_mul_f32 v[72:73], v[72:73], v[76:77]
	v_exp_f32_e32 v70, v70
	v_pk_mul_f32 v[74:75], v[74:75], v[78:79]
	v_exp_f32_e32 v71, v71
	v_pk_add_f32 v[76:77], v[76:77], 2.0 op_sel_hi:[1,0] neg_lo:[1,0] neg_hi:[1,0]
	v_pk_add_f32 v[68:69], v[68:69], 1.0 op_sel_hi:[1,0]
	v_pk_add_f32 v[78:79], v[78:79], 2.0 op_sel_hi:[1,0] neg_lo:[1,0] neg_hi:[1,0]
	v_pk_add_f32 v[70:71], v[70:71], 1.0 op_sel_hi:[1,0]
	v_pk_mul_f32 v[76:77], v[76:77], v[68:69]
	v_pk_mul_f32 v[68:69], v[68:69], v[72:73]
	v_pk_mul_f32 v[78:79], v[78:79], v[70:71]
	v_pk_mul_f32 v[70:71], v[70:71], v[74:75]
	v_rcp_f32_e32 v68, v68
	v_rcp_f32_e32 v69, v69
	v_rcp_f32_e32 v70, v70
	v_rcp_f32_e32 v71, v71
	s_waitcnt lgkmcnt(0)
	v_pk_fma_f32 v[76:77], v[160:161], v[72:73], v[76:77]
	v_pk_fma_f32 v[78:79], v[162:163], v[74:75], v[78:79]
	v_lshl_add_u64 v[72:73], v[176:177], 0, s[20:21]
	v_pk_mul_f32 v[68:69], v[68:69], v[76:77]
	v_pk_mul_f32 v[70:71], v[70:71], v[78:79]
	global_store_dwordx4 v[72:73], v[68:71], off nt
	s_nop 1
	v_pk_mul_f32 v[68:69], v[68:69], s[96:97] op_sel_hi:[1,0]
	v_pk_mul_f32 v[70:71], v[70:71], s[96:97] op_sel_hi:[1,0]
	v_exp_f32_e32 v64, v64
	v_exp_f32_e32 v65, v65
	v_exp_f32_e32 v66, v66
	v_pk_fma_f32 v[64:65], v[64:65], s[98:99], s[98:99] op_sel_hi:[1,0,0]
	v_exp_f32_e32 v67, v67
	v_exp_f32_e32 v68, v68
	v_pk_fma_f32 v[66:67], v[66:67], s[98:99], s[98:99] op_sel_hi:[1,0,0]
	v_exp_f32_e32 v69, v69
	v_exp_f32_e32 v70, v70
	v_pk_add_f32 v[68:69], v[68:69], 1.0 op_sel_hi:[1,0]
	v_exp_f32_e32 v71, v71
	v_pk_mul_f32 v[64:65], v[64:65], v[68:69]
	v_rcp_f32_e32 v64, v64
	v_pk_add_f32 v[70:71], v[70:71], 1.0 op_sel_hi:[1,0]
	v_rcp_f32_e32 v65, v65
	v_pk_mul_f32 v[66:67], v[66:67], v[70:71]
	v_pk_add_f32 v[68:69], v[68:69], 2.0 op_sel_hi:[1,0] neg_lo:[1,0] neg_hi:[1,0]
	v_rcp_f32_e32 v66, v66
	v_rcp_f32_e32 v67, v67
	v_pk_add_f32 v[70:71], v[70:71], 2.0 op_sel_hi:[1,0] neg_lo:[1,0] neg_hi:[1,0]
	v_pk_mul_f32 v[64:65], v[64:65], v[68:69]
	v_pk_mul_f32 v[66:67], v[66:67], v[70:71]
	v_ashrrev_i32_e32 v203, 31, v202
	v_cvt_pk_fp8_f32 v72, v64, v65
	s_and_b64 vcc, exec, s[0:1]
	v_cvt_pk_fp8_f32 v72, v66, v67 op_sel:[0,0,1]
	v_lshlrev_b64 v[68:69], 10, v[202:203]
	v_lshl_add_u64 v[70:71], v[122:123], 0, v[68:69]
	global_store_dword v[70:71], v72, off
	v_pk_mul_f32 v[64:65], v[64:65], s[98:99] op_sel_hi:[1,0]
	v_pk_mul_f32 v[66:67], v[66:67], s[98:99] op_sel_hi:[1,0]
	v_cvt_pk_f16_f32 v64, v64, v65
	v_cvt_pk_f16_f32 v65, v66, v67
	v_lshl_add_u64 v[66:67], v[68:69], 1, v[120:121]
	global_store_dwordx2 v[66:67], v[64:65], off
	v_exp_f32_e32 v56, v56
	v_exp_f32_e32 v57, v57
	v_exp_f32_e32 v58, v58
	v_pk_add_f32 v[56:57], v[56:57], 1.0 op_sel_hi:[1,0]
	v_exp_f32_e32 v59, v59
	v_exp_f32_e32 v60, v60
	v_pk_add_f32 v[58:59], v[58:59], 1.0 op_sel_hi:[1,0]
	v_exp_f32_e32 v61, v61
	v_exp_f32_e32 v62, v62
	v_pk_add_f32 v[60:61], v[60:61], 1.0 op_sel_hi:[1,0]
	v_exp_f32_e32 v63, v63
	v_exp_f32_e32 v52, v52
	v_pk_add_f32 v[62:63], v[62:63], 1.0 op_sel_hi:[1,0]
	v_exp_f32_e32 v53, v53
	v_pk_mul_f32 v[56:57], v[56:57], v[60:61]
	v_exp_f32_e32 v54, v54
	v_pk_mul_f32 v[58:59], v[58:59], v[62:63]
	v_exp_f32_e32 v55, v55
	v_pk_add_f32 v[60:61], v[60:61], 2.0 op_sel_hi:[1,0] neg_lo:[1,0] neg_hi:[1,0]
	v_pk_add_f32 v[52:53], v[52:53], 1.0 op_sel_hi:[1,0]
	v_pk_add_f32 v[62:63], v[62:63], 2.0 op_sel_hi:[1,0] neg_lo:[1,0] neg_hi:[1,0]
	v_pk_add_f32 v[54:55], v[54:55], 1.0 op_sel_hi:[1,0]
	v_pk_mul_f32 v[60:61], v[60:61], v[52:53]
	v_pk_mul_f32 v[52:53], v[52:53], v[56:57]
	v_pk_mul_f32 v[62:63], v[62:63], v[54:55]
	v_pk_mul_f32 v[54:55], v[54:55], v[58:59]
	v_rcp_f32_e32 v52, v52
	v_rcp_f32_e32 v53, v53
	v_rcp_f32_e32 v54, v54
	v_rcp_f32_e32 v55, v55
	s_waitcnt vmcnt(8)
	v_pk_fma_f32 v[60:61], v[156:157], v[56:57], v[60:61]
	v_pk_fma_f32 v[62:63], v[158:159], v[58:59], v[62:63]
	v_pk_mul_f32 v[52:53], v[52:53], v[60:61]
	v_pk_mul_f32 v[54:55], v[54:55], v[62:63]
	v_lshl_add_u64 v[56:57], v[176:177], 0, s[14:15]
	global_store_dwordx4 v[56:57], v[52:55], off nt
	s_nop 1
	v_pk_mul_f32 v[52:53], v[52:53], s[96:97] op_sel_hi:[1,0]
	v_pk_mul_f32 v[54:55], v[54:55], s[96:97] op_sel_hi:[1,0]
	v_exp_f32_e32 v48, v48
	v_exp_f32_e32 v49, v49
	v_exp_f32_e32 v50, v50
	v_pk_fma_f32 v[48:49], v[48:49], s[98:99], s[98:99] op_sel_hi:[1,0,0]
	v_exp_f32_e32 v51, v51
	v_exp_f32_e32 v52, v52
	v_pk_fma_f32 v[50:51], v[50:51], s[98:99], s[98:99] op_sel_hi:[1,0,0]
	v_exp_f32_e32 v53, v53
	v_exp_f32_e32 v54, v54
	v_pk_add_f32 v[52:53], v[52:53], 1.0 op_sel_hi:[1,0]
	v_exp_f32_e32 v55, v55
	v_pk_mul_f32 v[48:49], v[48:49], v[52:53]
	v_rcp_f32_e32 v48, v48
	v_pk_add_f32 v[54:55], v[54:55], 1.0 op_sel_hi:[1,0]
	v_rcp_f32_e32 v49, v49
	v_pk_mul_f32 v[50:51], v[50:51], v[54:55]
	v_pk_add_f32 v[52:53], v[52:53], 2.0 op_sel_hi:[1,0] neg_lo:[1,0] neg_hi:[1,0]
	v_rcp_f32_e32 v50, v50
	v_rcp_f32_e32 v51, v51
	v_pk_add_f32 v[54:55], v[54:55], 2.0 op_sel_hi:[1,0] neg_lo:[1,0] neg_hi:[1,0]
	v_pk_mul_f32 v[48:49], v[48:49], v[52:53]
	v_pk_mul_f32 v[50:51], v[50:51], v[54:55]
	v_ashrrev_i32_e32 v201, 31, v200
	v_cvt_pk_fp8_f32 v56, v48, v49
	s_and_b64 vcc, exec, s[0:1]
	v_cvt_pk_fp8_f32 v56, v50, v51 op_sel:[0,0,1]
	v_lshlrev_b64 v[52:53], 10, v[200:201]
	v_lshl_add_u64 v[54:55], v[122:123], 0, v[52:53]
	global_store_dword v[54:55], v56, off
	v_pk_mul_f32 v[48:49], v[48:49], s[98:99] op_sel_hi:[1,0]
	v_pk_mul_f32 v[50:51], v[50:51], s[98:99] op_sel_hi:[1,0]
	v_cvt_pk_f16_f32 v48, v48, v49
	v_cvt_pk_f16_f32 v49, v50, v51
	v_lshl_add_u64 v[50:51], v[52:53], 1, v[120:121]
	global_store_dwordx2 v[50:51], v[48:49], off
	v_exp_f32_e32 v40, v40
	v_exp_f32_e32 v41, v41
	v_exp_f32_e32 v42, v42
	v_pk_add_f32 v[40:41], v[40:41], 1.0 op_sel_hi:[1,0]
	v_exp_f32_e32 v43, v43
	v_exp_f32_e32 v44, v44
	v_pk_add_f32 v[42:43], v[42:43], 1.0 op_sel_hi:[1,0]
	v_exp_f32_e32 v45, v45
	v_exp_f32_e32 v46, v46
	v_pk_add_f32 v[44:45], v[44:45], 1.0 op_sel_hi:[1,0]
	v_exp_f32_e32 v47, v47
	v_exp_f32_e32 v36, v36
	v_pk_add_f32 v[46:47], v[46:47], 1.0 op_sel_hi:[1,0]
	v_exp_f32_e32 v37, v37
	v_pk_mul_f32 v[40:41], v[40:41], v[44:45]
	v_exp_f32_e32 v38, v38
	v_pk_mul_f32 v[42:43], v[42:43], v[46:47]
	v_exp_f32_e32 v39, v39
	v_pk_add_f32 v[44:45], v[44:45], 2.0 op_sel_hi:[1,0] neg_lo:[1,0] neg_hi:[1,0]
	v_pk_add_f32 v[36:37], v[36:37], 1.0 op_sel_hi:[1,0]
	v_pk_add_f32 v[46:47], v[46:47], 2.0 op_sel_hi:[1,0] neg_lo:[1,0] neg_hi:[1,0]
	v_pk_add_f32 v[38:39], v[38:39], 1.0 op_sel_hi:[1,0]
	v_pk_mul_f32 v[44:45], v[44:45], v[36:37]
	v_pk_mul_f32 v[36:37], v[36:37], v[40:41]
	v_pk_mul_f32 v[46:47], v[46:47], v[38:39]
	v_pk_mul_f32 v[38:39], v[38:39], v[42:43]
	v_rcp_f32_e32 v36, v36
	v_rcp_f32_e32 v37, v37
	v_rcp_f32_e32 v38, v38
	v_rcp_f32_e32 v39, v39
	v_pk_fma_f32 v[44:45], v[152:153], v[40:41], v[44:45]
	v_pk_fma_f32 v[46:47], v[154:155], v[42:43], v[46:47]
	v_lshl_add_u64 v[40:41], v[176:177], 0, s[22:23]
	v_pk_mul_f32 v[36:37], v[36:37], v[44:45]
	v_pk_mul_f32 v[38:39], v[38:39], v[46:47]
	global_store_dwordx4 v[40:41], v[36:39], off nt
	s_nop 1
	v_pk_mul_f32 v[36:37], v[36:37], s[96:97] op_sel_hi:[1,0]
	v_pk_mul_f32 v[38:39], v[38:39], s[96:97] op_sel_hi:[1,0]
	v_exp_f32_e32 v32, v32
	v_exp_f32_e32 v33, v33
	v_exp_f32_e32 v34, v34
	v_pk_fma_f32 v[32:33], v[32:33], s[98:99], s[98:99] op_sel_hi:[1,0,0]
	v_exp_f32_e32 v35, v35
	v_exp_f32_e32 v36, v36
	v_pk_fma_f32 v[34:35], v[34:35], s[98:99], s[98:99] op_sel_hi:[1,0,0]
	v_exp_f32_e32 v37, v37
	v_exp_f32_e32 v38, v38
	v_pk_add_f32 v[36:37], v[36:37], 1.0 op_sel_hi:[1,0]
	v_exp_f32_e32 v39, v39
	v_pk_mul_f32 v[32:33], v[32:33], v[36:37]
	v_rcp_f32_e32 v32, v32
	v_pk_add_f32 v[38:39], v[38:39], 1.0 op_sel_hi:[1,0]
	v_rcp_f32_e32 v33, v33
	v_pk_mul_f32 v[34:35], v[34:35], v[38:39]
	v_pk_add_f32 v[36:37], v[36:37], 2.0 op_sel_hi:[1,0] neg_lo:[1,0] neg_hi:[1,0]
	v_rcp_f32_e32 v34, v34
	v_rcp_f32_e32 v35, v35
	v_pk_add_f32 v[38:39], v[38:39], 2.0 op_sel_hi:[1,0] neg_lo:[1,0] neg_hi:[1,0]
	v_pk_mul_f32 v[32:33], v[32:33], v[36:37]
	v_pk_mul_f32 v[34:35], v[34:35], v[38:39]
	v_cvt_pk_fp8_f32 v40, v32, v33
	v_or_b32_e32 v36, 16, v200
	v_ashrrev_i32_e32 v37, 31, v36
	v_lshlrev_b64 v[36:37], 10, v[36:37]
	v_cvt_pk_fp8_f32 v40, v34, v35 op_sel:[0,0,1]
	v_lshl_add_u64 v[38:39], v[122:123], 0, v[36:37]
	global_store_dword v[38:39], v40, off
	v_pk_mul_f32 v[32:33], v[32:33], s[98:99] op_sel_hi:[1,0]
	v_pk_mul_f32 v[34:35], v[34:35], s[98:99] op_sel_hi:[1,0]
	v_cvt_pk_f16_f32 v32, v32, v33
	v_cvt_pk_f16_f32 v33, v34, v35
	v_lshl_add_u64 v[34:35], v[36:37], 1, v[120:121]
	global_store_dwordx2 v[34:35], v[32:33], off
	v_exp_f32_e32 v24, v24
	v_exp_f32_e32 v25, v25
	v_exp_f32_e32 v26, v26
	v_pk_add_f32 v[24:25], v[24:25], 1.0 op_sel_hi:[1,0]
	v_exp_f32_e32 v27, v27
	v_exp_f32_e32 v28, v28
	v_pk_add_f32 v[26:27], v[26:27], 1.0 op_sel_hi:[1,0]
	v_exp_f32_e32 v29, v29
	v_exp_f32_e32 v30, v30
	v_pk_add_f32 v[28:29], v[28:29], 1.0 op_sel_hi:[1,0]
	v_exp_f32_e32 v31, v31
	v_exp_f32_e32 v20, v20
	v_pk_add_f32 v[30:31], v[30:31], 1.0 op_sel_hi:[1,0]
	v_exp_f32_e32 v21, v21
	v_pk_mul_f32 v[24:25], v[24:25], v[28:29]
	v_exp_f32_e32 v22, v22
	v_pk_mul_f32 v[26:27], v[26:27], v[30:31]
	v_exp_f32_e32 v23, v23
	v_pk_add_f32 v[28:29], v[28:29], 2.0 op_sel_hi:[1,0] neg_lo:[1,0] neg_hi:[1,0]
	v_pk_add_f32 v[20:21], v[20:21], 1.0 op_sel_hi:[1,0]
	v_pk_add_f32 v[30:31], v[30:31], 2.0 op_sel_hi:[1,0] neg_lo:[1,0] neg_hi:[1,0]
	v_pk_add_f32 v[22:23], v[22:23], 1.0 op_sel_hi:[1,0]
	v_pk_mul_f32 v[28:29], v[28:29], v[20:21]
	v_pk_mul_f32 v[20:21], v[20:21], v[24:25]
	v_pk_mul_f32 v[30:31], v[30:31], v[22:23]
	v_pk_mul_f32 v[22:23], v[22:23], v[26:27]
	v_rcp_f32_e32 v20, v20
	v_rcp_f32_e32 v21, v21
	v_rcp_f32_e32 v22, v22
	v_rcp_f32_e32 v23, v23
	v_pk_fma_f32 v[28:29], v[148:149], v[24:25], v[28:29]
	v_pk_fma_f32 v[30:31], v[150:151], v[26:27], v[30:31]
	v_pk_mul_f32 v[20:21], v[20:21], v[28:29]
	v_pk_mul_f32 v[22:23], v[22:23], v[30:31]
	v_lshl_add_u64 v[24:25], v[176:177], 0, s[16:17]
	global_store_dwordx4 v[24:25], v[20:23], off nt
	s_nop 1
	v_pk_mul_f32 v[20:21], v[20:21], s[96:97] op_sel_hi:[1,0]
	v_pk_mul_f32 v[22:23], v[22:23], s[96:97] op_sel_hi:[1,0]
	v_exp_f32_e32 v16, v16
	v_exp_f32_e32 v17, v17
	v_exp_f32_e32 v18, v18
	v_pk_fma_f32 v[16:17], v[16:17], s[98:99], s[98:99] op_sel_hi:[1,0,0]
	v_exp_f32_e32 v19, v19
	v_exp_f32_e32 v20, v20
	v_pk_fma_f32 v[18:19], v[18:19], s[98:99], s[98:99] op_sel_hi:[1,0,0]
	v_exp_f32_e32 v21, v21
	v_exp_f32_e32 v22, v22
	v_pk_add_f32 v[20:21], v[20:21], 1.0 op_sel_hi:[1,0]
	v_exp_f32_e32 v23, v23
	v_pk_mul_f32 v[16:17], v[16:17], v[20:21]
	v_rcp_f32_e32 v16, v16
	v_pk_add_f32 v[22:23], v[22:23], 1.0 op_sel_hi:[1,0]
	v_rcp_f32_e32 v17, v17
	v_pk_mul_f32 v[18:19], v[18:19], v[22:23]
	v_pk_add_f32 v[20:21], v[20:21], 2.0 op_sel_hi:[1,0] neg_lo:[1,0] neg_hi:[1,0]
	v_rcp_f32_e32 v18, v18
	v_rcp_f32_e32 v19, v19
	v_pk_add_f32 v[22:23], v[22:23], 2.0 op_sel_hi:[1,0] neg_lo:[1,0] neg_hi:[1,0]
	v_pk_mul_f32 v[16:17], v[16:17], v[20:21]
	v_pk_mul_f32 v[18:19], v[18:19], v[22:23]
	v_cvt_pk_fp8_f32 v24, v16, v17
	v_or_b32_e32 v20, 32, v200
	v_ashrrev_i32_e32 v21, 31, v20
	v_lshlrev_b64 v[20:21], 10, v[20:21]
	v_cvt_pk_fp8_f32 v24, v18, v19 op_sel:[0,0,1]
	v_lshl_add_u64 v[22:23], v[122:123], 0, v[20:21]
	global_store_dword v[22:23], v24, off
	v_pk_mul_f32 v[16:17], v[16:17], s[98:99] op_sel_hi:[1,0]
	v_pk_mul_f32 v[18:19], v[18:19], s[98:99] op_sel_hi:[1,0]
	v_cvt_pk_f16_f32 v16, v16, v17
	v_cvt_pk_f16_f32 v17, v18, v19
	v_lshl_add_u64 v[18:19], v[20:21], 1, v[120:121]
	global_store_dwordx2 v[18:19], v[16:17], off
	v_exp_f32_e32 v8, v8
	v_exp_f32_e32 v9, v9
	v_exp_f32_e32 v10, v10
	v_pk_add_f32 v[8:9], v[8:9], 1.0 op_sel_hi:[1,0]
	v_exp_f32_e32 v11, v11
	v_exp_f32_e32 v12, v12
	v_pk_add_f32 v[10:11], v[10:11], 1.0 op_sel_hi:[1,0]
	v_exp_f32_e32 v13, v13
	v_exp_f32_e32 v14, v14
	v_pk_add_f32 v[12:13], v[12:13], 1.0 op_sel_hi:[1,0]
	v_exp_f32_e32 v15, v15
	v_exp_f32_e32 v4, v4
	v_pk_add_f32 v[14:15], v[14:15], 1.0 op_sel_hi:[1,0]
	v_exp_f32_e32 v5, v5
	v_pk_mul_f32 v[8:9], v[8:9], v[12:13]
	v_exp_f32_e32 v6, v6
	v_pk_mul_f32 v[10:11], v[10:11], v[14:15]
	v_exp_f32_e32 v7, v7
	v_pk_add_f32 v[12:13], v[12:13], 2.0 op_sel_hi:[1,0] neg_lo:[1,0] neg_hi:[1,0]
	v_pk_add_f32 v[4:5], v[4:5], 1.0 op_sel_hi:[1,0]
	v_pk_add_f32 v[14:15], v[14:15], 2.0 op_sel_hi:[1,0] neg_lo:[1,0] neg_hi:[1,0]
	v_pk_add_f32 v[6:7], v[6:7], 1.0 op_sel_hi:[1,0]
	v_pk_mul_f32 v[12:13], v[12:13], v[4:5]
	v_pk_mul_f32 v[4:5], v[4:5], v[8:9]
	v_pk_mul_f32 v[14:15], v[14:15], v[6:7]
	v_pk_mul_f32 v[6:7], v[6:7], v[10:11]
	v_rcp_f32_e32 v4, v4
	v_rcp_f32_e32 v5, v5
	v_rcp_f32_e32 v6, v6
	v_rcp_f32_e32 v7, v7
	v_pk_fma_f32 v[12:13], v[144:145], v[8:9], v[12:13]
	v_pk_fma_f32 v[14:15], v[146:147], v[10:11], v[14:15]
	v_lshl_add_u64 v[8:9], v[176:177], 0, s[24:25]
	v_pk_mul_f32 v[4:5], v[4:5], v[12:13]
	v_pk_mul_f32 v[6:7], v[6:7], v[14:15]
	global_store_dwordx4 v[8:9], v[4:7], off nt
	s_nop 1
	v_pk_mul_f32 v[4:5], v[4:5], s[96:97] op_sel_hi:[1,0]
	v_pk_mul_f32 v[6:7], v[6:7], s[96:97] op_sel_hi:[1,0]
	v_exp_f32_e32 v0, v0
	v_exp_f32_e32 v1, v1
	v_exp_f32_e32 v2, v2
	v_pk_fma_f32 v[0:1], v[0:1], s[98:99], s[98:99] op_sel_hi:[1,0,0]
	v_exp_f32_e32 v3, v3
	v_exp_f32_e32 v4, v4
	v_pk_fma_f32 v[2:3], v[2:3], s[98:99], s[98:99] op_sel_hi:[1,0,0]
	v_exp_f32_e32 v5, v5
	v_exp_f32_e32 v6, v6
	v_pk_add_f32 v[4:5], v[4:5], 1.0 op_sel_hi:[1,0]
	v_exp_f32_e32 v7, v7
	v_pk_mul_f32 v[0:1], v[0:1], v[4:5]
	v_rcp_f32_e32 v0, v0
	v_pk_add_f32 v[6:7], v[6:7], 1.0 op_sel_hi:[1,0]
	v_rcp_f32_e32 v1, v1
	v_pk_mul_f32 v[2:3], v[2:3], v[6:7]
	v_pk_add_f32 v[4:5], v[4:5], 2.0 op_sel_hi:[1,0] neg_lo:[1,0] neg_hi:[1,0]
	v_rcp_f32_e32 v2, v2
	v_rcp_f32_e32 v3, v3
	v_pk_add_f32 v[6:7], v[6:7], 2.0 op_sel_hi:[1,0] neg_lo:[1,0] neg_hi:[1,0]
	v_pk_mul_f32 v[0:1], v[0:1], v[4:5]
	v_pk_mul_f32 v[2:3], v[2:3], v[6:7]
	v_cvt_pk_fp8_f32 v8, v0, v1
	v_or_b32_e32 v4, 48, v200
	v_ashrrev_i32_e32 v5, 31, v4
	v_lshlrev_b64 v[4:5], 10, v[4:5]
	v_cvt_pk_fp8_f32 v8, v2, v3 op_sel:[0,0,1]
	v_lshl_add_u64 v[6:7], v[122:123], 0, v[4:5]
	global_store_dword v[6:7], v8, off
	v_pk_mul_f32 v[0:1], v[0:1], s[98:99] op_sel_hi:[1,0]
	v_pk_mul_f32 v[2:3], v[2:3], s[98:99] op_sel_hi:[1,0]
	v_cvt_pk_f16_f32 v0, v0, v1
	v_cvt_pk_f16_f32 v1, v2, v3
	v_lshl_add_u64 v[2:3], v[4:5], 1, v[120:121]
	global_store_dwordx2 v[2:3], v[0:1], off
	s_branch .LBB2_24
.Lmy_epi_last:
	s_cmp_eq_u32 s30, 7
	s_cbranch_scc1 .Lmy_epi_l7
	v_exp_f32_e32 v120, v120
	v_exp_f32_e32 v121, v121
	v_exp_f32_e32 v122, v122
	v_pk_add_f32 v[120:121], v[120:121], 1.0 op_sel_hi:[1,0]
	v_exp_f32_e32 v123, v123
	v_exp_f32_e32 v124, v124
	v_pk_add_f32 v[122:123], v[122:123], 1.0 op_sel_hi:[1,0]
	v_exp_f32_e32 v125, v125
	v_exp_f32_e32 v126, v126
	v_pk_add_f32 v[124:125], v[124:125], 1.0 op_sel_hi:[1,0]
	v_exp_f32_e32 v127, v127
	v_exp_f32_e32 v116, v116
	v_pk_add_f32 v[126:127], v[126:127], 1.0 op_sel_hi:[1,0]
	v_exp_f32_e32 v117, v117
	v_pk_mul_f32 v[120:121], v[120:121], v[124:125]
	v_exp_f32_e32 v118, v118
	v_pk_mul_f32 v[122:123], v[122:123], v[126:127]
	v_exp_f32_e32 v119, v119
	v_pk_add_f32 v[124:125], v[124:125], 2.0 op_sel_hi:[1,0] neg_lo:[1,0] neg_hi:[1,0]
	v_pk_add_f32 v[116:117], v[116:117], 1.0 op_sel_hi:[1,0]
	v_pk_add_f32 v[126:127], v[126:127], 2.0 op_sel_hi:[1,0] neg_lo:[1,0] neg_hi:[1,0]
	v_pk_add_f32 v[118:119], v[118:119], 1.0 op_sel_hi:[1,0]
	v_pk_mul_f32 v[124:125], v[124:125], v[116:117]
	v_pk_mul_f32 v[116:117], v[116:117], v[120:121]
	v_pk_mul_f32 v[126:127], v[126:127], v[118:119]
	v_pk_mul_f32 v[118:119], v[118:119], v[122:123]
	v_rcp_f32_e32 v116, v116
	v_rcp_f32_e32 v117, v117
	v_rcp_f32_e32 v118, v118
	v_rcp_f32_e32 v119, v119
	s_waitcnt lgkmcnt(3)
	v_pk_fma_f32 v[124:125], v[172:173], v[120:121], v[124:125]
	v_pk_fma_f32 v[126:127], v[174:175], v[122:123], v[126:127]
	v_pk_mul_f32 v[116:117], v[116:117], v[124:125]
	v_pk_mul_f32 v[118:119], v[118:119], v[126:127]
	global_store_dwordx4 v[176:177], v[116:119], off sc1
	s_nop 1
	v_pk_mul_f32 v[116:117], v[116:117], s[96:97] op_sel_hi:[1,0]
	v_pk_mul_f32 v[118:119], v[118:119], s[96:97] op_sel_hi:[1,0]
	v_exp_f32_e32 v112, v112
	v_exp_f32_e32 v113, v113
	v_exp_f32_e32 v114, v114
	v_pk_fma_f32 v[112:113], v[112:113], s[98:99], s[98:99] op_sel_hi:[1,0,0]
	v_exp_f32_e32 v115, v115
	v_exp_f32_e32 v116, v116
	v_pk_fma_f32 v[114:115], v[114:115], s[98:99], s[98:99] op_sel_hi:[1,0,0]
	v_exp_f32_e32 v117, v117
	v_exp_f32_e32 v118, v118
	v_pk_add_f32 v[116:117], v[116:117], 1.0 op_sel_hi:[1,0]
	v_exp_f32_e32 v119, v119
	v_pk_mul_f32 v[112:113], v[112:113], v[116:117]
	v_rcp_f32_e32 v112, v112
	v_pk_add_f32 v[118:119], v[118:119], 1.0 op_sel_hi:[1,0]
	v_rcp_f32_e32 v113, v113
	v_pk_mul_f32 v[114:115], v[114:115], v[118:119]
	v_pk_add_f32 v[116:117], v[116:117], 2.0 op_sel_hi:[1,0] neg_lo:[1,0] neg_hi:[1,0]
	v_rcp_f32_e32 v114, v114
	v_rcp_f32_e32 v115, v115
	v_pk_add_f32 v[118:119], v[118:119], 2.0 op_sel_hi:[1,0] neg_lo:[1,0] neg_hi:[1,0]
	v_pk_mul_f32 v[112:113], v[112:113], v[116:117]
	v_pk_mul_f32 v[114:115], v[114:115], v[118:119]
	v_cvt_pk_fp8_f32 v124, v112, v113
	s_add_u32 s0, s8, s27
	s_addc_u32 s1, s9, 0
	s_ashr_i32 s35, s34, 31
	s_lshl_b64 s[34:35], s[34:35], 21
	v_ashrrev_i32_e32 v209, 31, v208
	s_add_u32 s36, s73, s34
	v_lshrrev_b32_e32 v126, 4, v210
	v_and_b32_e32 v127, 15, v210
	v_lshl_or_b32 v126, v126, 8, v127
	v_and_b32_e32 v127, 15, v208
	v_mul_u32_u24_e32 v127, 0x3f0, v127
	v_sub_u32_e32 v126, v126, v127
	v_ashrrev_i32_e32 v127, 31, v126
	v_lshl_add_u64 v[122:123], s[0:1], 0, v[126:127]
	v_cvt_pk_fp8_f32 v124, v114, v115 op_sel:[0,0,1]
	v_lshlrev_b64 v[116:117], 10, v[208:209]
	s_addc_u32 s37, s74, s35
	v_lshl_add_u64 v[118:119], v[122:123], 0, v[116:117]
	global_store_dword v[118:119], v124, off
	s_cmp_eq_u32 s30, 7
	s_cselect_b64 s[34:35], -1, 0
	s_cmp_lg_u32 s30, 7
	v_lshrrev_b32_e32 v126, 4, v210
	v_lshlrev_b32_e32 v126, 9, v126
	v_and_b32_e32 v127, 15, v210
	v_lshl_or_b32 v126, v127, 1, v126
	v_and_b32_e32 v127, 15, v208
	v_mul_u32_u24_e32 v127, 0x7e0, v127
	v_sub_u32_e32 v126, v126, v127
	v_ashrrev_i32_e32 v127, 31, v126
	v_lshl_add_u64 v[120:121], s[36:37], 0, v[126:127]
	v_exp_f32_e32 v104, v104
	v_exp_f32_e32 v105, v105
	v_exp_f32_e32 v106, v106
	v_pk_add_f32 v[104:105], v[104:105], 1.0 op_sel_hi:[1,0]
	v_exp_f32_e32 v107, v107
	v_exp_f32_e32 v108, v108
	v_pk_add_f32 v[106:107], v[106:107], 1.0 op_sel_hi:[1,0]
	v_exp_f32_e32 v109, v109
	v_exp_f32_e32 v110, v110
	v_pk_add_f32 v[108:109], v[108:109], 1.0 op_sel_hi:[1,0]
	v_exp_f32_e32 v111, v111
	v_exp_f32_e32 v100, v100
	v_pk_add_f32 v[110:111], v[110:111], 1.0 op_sel_hi:[1,0]
	v_exp_f32_e32 v101, v101
	v_pk_mul_f32 v[104:105], v[104:105], v[108:109]
	v_exp_f32_e32 v102, v102
	v_pk_mul_f32 v[106:107], v[106:107], v[110:111]
	v_exp_f32_e32 v103, v103
	v_pk_add_f32 v[108:109], v[108:109], 2.0 op_sel_hi:[1,0] neg_lo:[1,0] neg_hi:[1,0]
	v_pk_add_f32 v[100:101], v[100:101], 1.0 op_sel_hi:[1,0]
	v_pk_add_f32 v[110:111], v[110:111], 2.0 op_sel_hi:[1,0] neg_lo:[1,0] neg_hi:[1,0]
	v_pk_add_f32 v[102:103], v[102:103], 1.0 op_sel_hi:[1,0]
	v_pk_mul_f32 v[108:109], v[108:109], v[100:101]
	v_pk_mul_f32 v[100:101], v[100:101], v[104:105]
	v_pk_mul_f32 v[110:111], v[110:111], v[102:103]
	v_pk_mul_f32 v[102:103], v[102:103], v[106:107]
	v_rcp_f32_e32 v100, v100
	v_rcp_f32_e32 v101, v101
	v_rcp_f32_e32 v102, v102
	v_rcp_f32_e32 v103, v103
	s_waitcnt lgkmcnt(2)
	v_pk_fma_f32 v[108:109], v[168:169], v[104:105], v[108:109]
	v_pk_fma_f32 v[110:111], v[170:171], v[106:107], v[110:111]
	v_lshl_add_u64 v[104:105], v[176:177], 0, s[18:19]
	v_pk_mul_f32 v[100:101], v[100:101], v[108:109]
	v_pk_mul_f32 v[102:103], v[102:103], v[110:111]
	global_store_dwordx4 v[104:105], v[100:103], off sc1
	s_nop 1
	v_pk_mul_f32 v[100:101], v[100:101], s[96:97] op_sel_hi:[1,0]
	v_pk_mul_f32 v[102:103], v[102:103], s[96:97] op_sel_hi:[1,0]
	v_exp_f32_e32 v96, v96
	v_exp_f32_e32 v97, v97
	v_exp_f32_e32 v98, v98
	v_pk_fma_f32 v[96:97], v[96:97], s[98:99], s[98:99] op_sel_hi:[1,0,0]
	v_exp_f32_e32 v99, v99
	v_exp_f32_e32 v100, v100
	v_pk_fma_f32 v[98:99], v[98:99], s[98:99], s[98:99] op_sel_hi:[1,0,0]
	v_exp_f32_e32 v101, v101
	v_exp_f32_e32 v102, v102
	v_pk_add_f32 v[100:101], v[100:101], 1.0 op_sel_hi:[1,0]
	v_exp_f32_e32 v103, v103
	v_pk_mul_f32 v[96:97], v[96:97], v[100:101]
	v_rcp_f32_e32 v96, v96
	v_pk_add_f32 v[102:103], v[102:103], 1.0 op_sel_hi:[1,0]
	v_rcp_f32_e32 v97, v97
	v_pk_mul_f32 v[98:99], v[98:99], v[102:103]
	v_pk_add_f32 v[100:101], v[100:101], 2.0 op_sel_hi:[1,0] neg_lo:[1,0] neg_hi:[1,0]
	v_rcp_f32_e32 v98, v98
	v_rcp_f32_e32 v99, v99
	v_pk_add_f32 v[102:103], v[102:103], 2.0 op_sel_hi:[1,0] neg_lo:[1,0] neg_hi:[1,0]
	v_pk_mul_f32 v[96:97], v[96:97], v[100:101]
	v_pk_mul_f32 v[98:99], v[98:99], v[102:103]
	v_cvt_pk_fp8_f32 v104, v96, v97
	v_ashrrev_i32_e32 v207, 31, v206
	v_lshlrev_b64 v[100:101], 10, v[206:207]
	v_lshl_add_u64 v[102:103], v[122:123], 0, v[100:101]
	v_cvt_pk_fp8_f32 v104, v98, v99 op_sel:[0,0,1]
	v_cndmask_b32_e64 v105, 0, 1, s[34:35]
	global_store_dword v[102:103], v104, off
	v_cmp_ne_u32_e64 s[0:1], 1, v105
	v_exp_f32_e32 v88, v88
	v_exp_f32_e32 v89, v89
	v_exp_f32_e32 v90, v90
	v_pk_add_f32 v[88:89], v[88:89], 1.0 op_sel_hi:[1,0]
	v_exp_f32_e32 v91, v91
	v_exp_f32_e32 v92, v92
	v_pk_add_f32 v[90:91], v[90:91], 1.0 op_sel_hi:[1,0]
	v_exp_f32_e32 v93, v93
	v_exp_f32_e32 v94, v94
	v_pk_add_f32 v[92:93], v[92:93], 1.0 op_sel_hi:[1,0]
	v_exp_f32_e32 v95, v95
	v_exp_f32_e32 v84, v84
	v_pk_add_f32 v[94:95], v[94:95], 1.0 op_sel_hi:[1,0]
	v_exp_f32_e32 v85, v85
	v_pk_mul_f32 v[88:89], v[88:89], v[92:93]
	v_exp_f32_e32 v86, v86
	v_pk_mul_f32 v[90:91], v[90:91], v[94:95]
	v_exp_f32_e32 v87, v87
	v_pk_add_f32 v[92:93], v[92:93], 2.0 op_sel_hi:[1,0] neg_lo:[1,0] neg_hi:[1,0]
	v_pk_add_f32 v[84:85], v[84:85], 1.0 op_sel_hi:[1,0]
	v_pk_add_f32 v[94:95], v[94:95], 2.0 op_sel_hi:[1,0] neg_lo:[1,0] neg_hi:[1,0]
	v_pk_add_f32 v[86:87], v[86:87], 1.0 op_sel_hi:[1,0]
	v_pk_mul_f32 v[92:93], v[92:93], v[84:85]
	v_pk_mul_f32 v[84:85], v[84:85], v[88:89]
	v_pk_mul_f32 v[94:95], v[94:95], v[86:87]
	v_pk_mul_f32 v[86:87], v[86:87], v[90:91]
	v_rcp_f32_e32 v84, v84
	v_rcp_f32_e32 v85, v85
	v_rcp_f32_e32 v86, v86
	v_rcp_f32_e32 v87, v87
	s_waitcnt lgkmcnt(1)
	v_pk_fma_f32 v[92:93], v[164:165], v[88:89], v[92:93]
	v_pk_fma_f32 v[94:95], v[166:167], v[90:91], v[94:95]
	v_pk_mul_f32 v[84:85], v[84:85], v[92:93]
	v_pk_mul_f32 v[86:87], v[86:87], v[94:95]
	v_lshl_add_u64 v[88:89], v[176:177], 0, s[12:13]
	global_store_dwordx4 v[88:89], v[84:87], off sc1
	s_nop 1
	v_pk_mul_f32 v[84:85], v[84:85], s[96:97] op_sel_hi:[1,0]
	v_pk_mul_f32 v[86:87], v[86:87], s[96:97] op_sel_hi:[1,0]
	v_exp_f32_e32 v80, v80
	v_exp_f32_e32 v81, v81
	v_exp_f32_e32 v82, v82
	v_pk_fma_f32 v[80:81], v[80:81], s[98:99], s[98:99] op_sel_hi:[1,0,0]
	v_exp_f32_e32 v83, v83
	v_exp_f32_e32 v84, v84
	v_pk_fma_f32 v[82:83], v[82:83], s[98:99], s[98:99] op_sel_hi:[1,0,0]
	v_exp_f32_e32 v85, v85
	v_exp_f32_e32 v86, v86
	v_pk_add_f32 v[84:85], v[84:85], 1.0 op_sel_hi:[1,0]
	v_exp_f32_e32 v87, v87
	v_pk_mul_f32 v[80:81], v[80:81], v[84:85]
	v_rcp_f32_e32 v80, v80
	v_pk_add_f32 v[86:87], v[86:87], 1.0 op_sel_hi:[1,0]
	v_rcp_f32_e32 v81, v81
	v_pk_mul_f32 v[82:83], v[82:83], v[86:87]
	v_pk_add_f32 v[84:85], v[84:85], 2.0 op_sel_hi:[1,0] neg_lo:[1,0] neg_hi:[1,0]
	v_rcp_f32_e32 v82, v82
	v_rcp_f32_e32 v83, v83
	v_pk_add_f32 v[86:87], v[86:87], 2.0 op_sel_hi:[1,0] neg_lo:[1,0] neg_hi:[1,0]
	v_pk_mul_f32 v[80:81], v[80:81], v[84:85]
	v_pk_mul_f32 v[82:83], v[82:83], v[86:87]
	v_ashrrev_i32_e32 v205, 31, v204
	v_cvt_pk_fp8_f32 v88, v80, v81
	s_and_b64 vcc, exec, s[0:1]
	v_cvt_pk_fp8_f32 v88, v82, v83 op_sel:[0,0,1]
	v_lshlrev_b64 v[84:85], 10, v[204:205]
	v_lshl_add_u64 v[86:87], v[122:123], 0, v[84:85]
	global_store_dword v[86:87], v88, off
	v_exp_f32_e32 v72, v72
	v_exp_f32_e32 v73, v73
	v_exp_f32_e32 v74, v74
	v_pk_add_f32 v[72:73], v[72:73], 1.0 op_sel_hi:[1,0]
	v_exp_f32_e32 v75, v75
	v_exp_f32_e32 v76, v76
	v_pk_add_f32 v[74:75], v[74:75], 1.0 op_sel_hi:[1,0]
	v_exp_f32_e32 v77, v77
	v_exp_f32_e32 v78, v78
	v_pk_add_f32 v[76:77], v[76:77], 1.0 op_sel_hi:[1,0]
	v_exp_f32_e32 v79, v79
	v_exp_f32_e32 v68, v68
	v_pk_add_f32 v[78:79], v[78:79], 1.0 op_sel_hi:[1,0]
	v_exp_f32_e32 v69, v69
	v_pk_mul_f32 v[72:73], v[72:73], v[76:77]
	v_exp_f32_e32 v70, v70
	v_pk_mul_f32 v[74:75], v[74:75], v[78:79]
	v_exp_f32_e32 v71, v71
	v_pk_add_f32 v[76:77], v[76:77], 2.0 op_sel_hi:[1,0] neg_lo:[1,0] neg_hi:[1,0]
	v_pk_add_f32 v[68:69], v[68:69], 1.0 op_sel_hi:[1,0]
	v_pk_add_f32 v[78:79], v[78:79], 2.0 op_sel_hi:[1,0] neg_lo:[1,0] neg_hi:[1,0]
	v_pk_add_f32 v[70:71], v[70:71], 1.0 op_sel_hi:[1,0]
	v_pk_mul_f32 v[76:77], v[76:77], v[68:69]
	v_pk_mul_f32 v[68:69], v[68:69], v[72:73]
	v_pk_mul_f32 v[78:79], v[78:79], v[70:71]
	v_pk_mul_f32 v[70:71], v[70:71], v[74:75]
	v_rcp_f32_e32 v68, v68
	v_rcp_f32_e32 v69, v69
	v_rcp_f32_e32 v70, v70
	v_rcp_f32_e32 v71, v71
	s_waitcnt lgkmcnt(0)
	v_pk_fma_f32 v[76:77], v[160:161], v[72:73], v[76:77]
	v_pk_fma_f32 v[78:79], v[162:163], v[74:75], v[78:79]
	v_lshl_add_u64 v[72:73], v[176:177], 0, s[20:21]
	v_pk_mul_f32 v[68:69], v[68:69], v[76:77]
	v_pk_mul_f32 v[70:71], v[70:71], v[78:79]
	global_store_dwordx4 v[72:73], v[68:71], off sc1
	s_nop 1
	v_pk_mul_f32 v[68:69], v[68:69], s[96:97] op_sel_hi:[1,0]
	v_pk_mul_f32 v[70:71], v[70:71], s[96:97] op_sel_hi:[1,0]
	v_exp_f32_e32 v64, v64
	v_exp_f32_e32 v65, v65
	v_exp_f32_e32 v66, v66
	v_pk_fma_f32 v[64:65], v[64:65], s[98:99], s[98:99] op_sel_hi:[1,0,0]
	v_exp_f32_e32 v67, v67
	v_exp_f32_e32 v68, v68
	v_pk_fma_f32 v[66:67], v[66:67], s[98:99], s[98:99] op_sel_hi:[1,0,0]
	v_exp_f32_e32 v69, v69
	v_exp_f32_e32 v70, v70
	v_pk_add_f32 v[68:69], v[68:69], 1.0 op_sel_hi:[1,0]
	v_exp_f32_e32 v71, v71
	v_pk_mul_f32 v[64:65], v[64:65], v[68:69]
	v_rcp_f32_e32 v64, v64
	v_pk_add_f32 v[70:71], v[70:71], 1.0 op_sel_hi:[1,0]
	v_rcp_f32_e32 v65, v65
	v_pk_mul_f32 v[66:67], v[66:67], v[70:71]
	v_pk_add_f32 v[68:69], v[68:69], 2.0 op_sel_hi:[1,0] neg_lo:[1,0] neg_hi:[1,0]
	v_rcp_f32_e32 v66, v66
	v_rcp_f32_e32 v67, v67
	v_pk_add_f32 v[70:71], v[70:71], 2.0 op_sel_hi:[1,0] neg_lo:[1,0] neg_hi:[1,0]
	v_pk_mul_f32 v[64:65], v[64:65], v[68:69]
	v_pk_mul_f32 v[66:67], v[66:67], v[70:71]
	v_ashrrev_i32_e32 v203, 31, v202
	v_cvt_pk_fp8_f32 v72, v64, v65
	s_and_b64 vcc, exec, s[0:1]
	v_cvt_pk_fp8_f32 v72, v66, v67 op_sel:[0,0,1]
	v_lshlrev_b64 v[68:69], 10, v[202:203]
	v_lshl_add_u64 v[70:71], v[122:123], 0, v[68:69]
	global_store_dword v[70:71], v72, off
	v_exp_f32_e32 v56, v56
	v_exp_f32_e32 v57, v57
	v_exp_f32_e32 v58, v58
	v_pk_add_f32 v[56:57], v[56:57], 1.0 op_sel_hi:[1,0]
	v_exp_f32_e32 v59, v59
	v_exp_f32_e32 v60, v60
	v_pk_add_f32 v[58:59], v[58:59], 1.0 op_sel_hi:[1,0]
	v_exp_f32_e32 v61, v61
	v_exp_f32_e32 v62, v62
	v_pk_add_f32 v[60:61], v[60:61], 1.0 op_sel_hi:[1,0]
	v_exp_f32_e32 v63, v63
	v_exp_f32_e32 v52, v52
	v_pk_add_f32 v[62:63], v[62:63], 1.0 op_sel_hi:[1,0]
	v_exp_f32_e32 v53, v53
	v_pk_mul_f32 v[56:57], v[56:57], v[60:61]
	v_exp_f32_e32 v54, v54
	v_pk_mul_f32 v[58:59], v[58:59], v[62:63]
	v_exp_f32_e32 v55, v55
	v_pk_add_f32 v[60:61], v[60:61], 2.0 op_sel_hi:[1,0] neg_lo:[1,0] neg_hi:[1,0]
	v_pk_add_f32 v[52:53], v[52:53], 1.0 op_sel_hi:[1,0]
	v_pk_add_f32 v[62:63], v[62:63], 2.0 op_sel_hi:[1,0] neg_lo:[1,0] neg_hi:[1,0]
	v_pk_add_f32 v[54:55], v[54:55], 1.0 op_sel_hi:[1,0]
	v_pk_mul_f32 v[60:61], v[60:61], v[52:53]
	v_pk_mul_f32 v[52:53], v[52:53], v[56:57]
	v_pk_mul_f32 v[62:63], v[62:63], v[54:55]
	v_pk_mul_f32 v[54:55], v[54:55], v[58:59]
	v_rcp_f32_e32 v52, v52
	v_rcp_f32_e32 v53, v53
	v_rcp_f32_e32 v54, v54
	v_rcp_f32_e32 v55, v55
	s_waitcnt vmcnt(8)
	v_pk_fma_f32 v[60:61], v[156:157], v[56:57], v[60:61]
	v_pk_fma_f32 v[62:63], v[158:159], v[58:59], v[62:63]
	v_pk_mul_f32 v[52:53], v[52:53], v[60:61]
	v_pk_mul_f32 v[54:55], v[54:55], v[62:63]
	v_lshl_add_u64 v[56:57], v[176:177], 0, s[14:15]
	global_store_dwordx4 v[56:57], v[52:55], off sc1
	s_nop 1
	v_pk_mul_f32 v[52:53], v[52:53], s[96:97] op_sel_hi:[1,0]
	v_pk_mul_f32 v[54:55], v[54:55], s[96:97] op_sel_hi:[1,0]
	v_exp_f32_e32 v48, v48
	v_exp_f32_e32 v49, v49
	v_exp_f32_e32 v50, v50
	v_pk_fma_f32 v[48:49], v[48:49], s[98:99], s[98:99] op_sel_hi:[1,0,0]
	v_exp_f32_e32 v51, v51
	v_exp_f32_e32 v52, v52
	v_pk_fma_f32 v[50:51], v[50:51], s[98:99], s[98:99] op_sel_hi:[1,0,0]
	v_exp_f32_e32 v53, v53
	v_exp_f32_e32 v54, v54
	v_pk_add_f32 v[52:53], v[52:53], 1.0 op_sel_hi:[1,0]
	v_exp_f32_e32 v55, v55
	v_pk_mul_f32 v[48:49], v[48:49], v[52:53]
	v_rcp_f32_e32 v48, v48
	v_pk_add_f32 v[54:55], v[54:55], 1.0 op_sel_hi:[1,0]
	v_rcp_f32_e32 v49, v49
	v_pk_mul_f32 v[50:51], v[50:51], v[54:55]
	v_pk_add_f32 v[52:53], v[52:53], 2.0 op_sel_hi:[1,0] neg_lo:[1,0] neg_hi:[1,0]
	v_rcp_f32_e32 v50, v50
	v_rcp_f32_e32 v51, v51
	v_pk_add_f32 v[54:55], v[54:55], 2.0 op_sel_hi:[1,0] neg_lo:[1,0] neg_hi:[1,0]
	v_pk_mul_f32 v[48:49], v[48:49], v[52:53]
	v_pk_mul_f32 v[50:51], v[50:51], v[54:55]
	v_ashrrev_i32_e32 v201, 31, v200
	v_cvt_pk_fp8_f32 v56, v48, v49
	s_and_b64 vcc, exec, s[0:1]
	v_cvt_pk_fp8_f32 v56, v50, v51 op_sel:[0,0,1]
	v_lshlrev_b64 v[52:53], 10, v[200:201]
	v_lshl_add_u64 v[54:55], v[122:123], 0, v[52:53]
	global_store_dword v[54:55], v56, off
	v_exp_f32_e32 v40, v40
	v_exp_f32_e32 v41, v41
	v_exp_f32_e32 v42, v42
	v_pk_add_f32 v[40:41], v[40:41], 1.0 op_sel_hi:[1,0]
	v_exp_f32_e32 v43, v43
	v_exp_f32_e32 v44, v44
	v_pk_add_f32 v[42:43], v[42:43], 1.0 op_sel_hi:[1,0]
	v_exp_f32_e32 v45, v45
	v_exp_f32_e32 v46, v46
	v_pk_add_f32 v[44:45], v[44:45], 1.0 op_sel_hi:[1,0]
	v_exp_f32_e32 v47, v47
	v_exp_f32_e32 v36, v36
	v_pk_add_f32 v[46:47], v[46:47], 1.0 op_sel_hi:[1,0]
	v_exp_f32_e32 v37, v37
	v_pk_mul_f32 v[40:41], v[40:41], v[44:45]
	v_exp_f32_e32 v38, v38
	v_pk_mul_f32 v[42:43], v[42:43], v[46:47]
	v_exp_f32_e32 v39, v39
	v_pk_add_f32 v[44:45], v[44:45], 2.0 op_sel_hi:[1,0] neg_lo:[1,0] neg_hi:[1,0]
	v_pk_add_f32 v[36:37], v[36:37], 1.0 op_sel_hi:[1,0]
	v_pk_add_f32 v[46:47], v[46:47], 2.0 op_sel_hi:[1,0] neg_lo:[1,0] neg_hi:[1,0]
	v_pk_add_f32 v[38:39], v[38:39], 1.0 op_sel_hi:[1,0]
	v_pk_mul_f32 v[44:45], v[44:45], v[36:37]
	v_pk_mul_f32 v[36:37], v[36:37], v[40:41]
	v_pk_mul_f32 v[46:47], v[46:47], v[38:39]
	v_pk_mul_f32 v[38:39], v[38:39], v[42:43]
	v_rcp_f32_e32 v36, v36
	v_rcp_f32_e32 v37, v37
	v_rcp_f32_e32 v38, v38
	v_rcp_f32_e32 v39, v39
	v_pk_fma_f32 v[44:45], v[152:153], v[40:41], v[44:45]
	v_pk_fma_f32 v[46:47], v[154:155], v[42:43], v[46:47]
	v_lshl_add_u64 v[40:41], v[176:177], 0, s[22:23]
	v_pk_mul_f32 v[36:37], v[36:37], v[44:45]
	v_pk_mul_f32 v[38:39], v[38:39], v[46:47]
	global_store_dwordx4 v[40:41], v[36:39], off sc1
	s_nop 1
	v_pk_mul_f32 v[36:37], v[36:37], s[96:97] op_sel_hi:[1,0]
	v_pk_mul_f32 v[38:39], v[38:39], s[96:97] op_sel_hi:[1,0]
	v_exp_f32_e32 v32, v32
	v_exp_f32_e32 v33, v33
	v_exp_f32_e32 v34, v34
	v_pk_fma_f32 v[32:33], v[32:33], s[98:99], s[98:99] op_sel_hi:[1,0,0]
	v_exp_f32_e32 v35, v35
	v_exp_f32_e32 v36, v36
	v_pk_fma_f32 v[34:35], v[34:35], s[98:99], s[98:99] op_sel_hi:[1,0,0]
	v_exp_f32_e32 v37, v37
	v_exp_f32_e32 v38, v38
	v_pk_add_f32 v[36:37], v[36:37], 1.0 op_sel_hi:[1,0]
	v_exp_f32_e32 v39, v39
	v_pk_mul_f32 v[32:33], v[32:33], v[36:37]
	v_rcp_f32_e32 v32, v32
	v_pk_add_f32 v[38:39], v[38:39], 1.0 op_sel_hi:[1,0]
	v_rcp_f32_e32 v33, v33
	v_pk_mul_f32 v[34:35], v[34:35], v[38:39]
	v_pk_add_f32 v[36:37], v[36:37], 2.0 op_sel_hi:[1,0] neg_lo:[1,0] neg_hi:[1,0]
	v_rcp_f32_e32 v34, v34
	v_rcp_f32_e32 v35, v35
	v_pk_add_f32 v[38:39], v[38:39], 2.0 op_sel_hi:[1,0] neg_lo:[1,0] neg_hi:[1,0]
	v_pk_mul_f32 v[32:33], v[32:33], v[36:37]
	v_pk_mul_f32 v[34:35], v[34:35], v[38:39]
	v_cvt_pk_fp8_f32 v40, v32, v33
	v_or_b32_e32 v36, 16, v200
	v_ashrrev_i32_e32 v37, 31, v36
	v_lshlrev_b64 v[36:37], 10, v[36:37]
	v_cvt_pk_fp8_f32 v40, v34, v35 op_sel:[0,0,1]
	v_lshl_add_u64 v[38:39], v[122:123], 0, v[36:37]
	global_store_dword v[38:39], v40, off
	v_exp_f32_e32 v24, v24
	v_exp_f32_e32 v25, v25
	v_exp_f32_e32 v26, v26
	v_pk_add_f32 v[24:25], v[24:25], 1.0 op_sel_hi:[1,0]
	v_exp_f32_e32 v27, v27
	v_exp_f32_e32 v28, v28
	v_pk_add_f32 v[26:27], v[26:27], 1.0 op_sel_hi:[1,0]
	v_exp_f32_e32 v29, v29
	v_exp_f32_e32 v30, v30
	v_pk_add_f32 v[28:29], v[28:29], 1.0 op_sel_hi:[1,0]
	v_exp_f32_e32 v31, v31
	v_exp_f32_e32 v20, v20
	v_pk_add_f32 v[30:31], v[30:31], 1.0 op_sel_hi:[1,0]
	v_exp_f32_e32 v21, v21
	v_pk_mul_f32 v[24:25], v[24:25], v[28:29]
	v_exp_f32_e32 v22, v22
	v_pk_mul_f32 v[26:27], v[26:27], v[30:31]
	v_exp_f32_e32 v23, v23
	v_pk_add_f32 v[28:29], v[28:29], 2.0 op_sel_hi:[1,0] neg_lo:[1,0] neg_hi:[1,0]
	v_pk_add_f32 v[20:21], v[20:21], 1.0 op_sel_hi:[1,0]
	v_pk_add_f32 v[30:31], v[30:31], 2.0 op_sel_hi:[1,0] neg_lo:[1,0] neg_hi:[1,0]
	v_pk_add_f32 v[22:23], v[22:23], 1.0 op_sel_hi:[1,0]
	v_pk_mul_f32 v[28:29], v[28:29], v[20:21]
	v_pk_mul_f32 v[20:21], v[20:21], v[24:25]
	v_pk_mul_f32 v[30:31], v[30:31], v[22:23]
	v_pk_mul_f32 v[22:23], v[22:23], v[26:27]
	v_rcp_f32_e32 v20, v20
	v_rcp_f32_e32 v21, v21
	v_rcp_f32_e32 v22, v22
	v_rcp_f32_e32 v23, v23
	v_pk_fma_f32 v[28:29], v[148:149], v[24:25], v[28:29]
	v_pk_fma_f32 v[30:31], v[150:151], v[26:27], v[30:31]
	v_pk_mul_f32 v[20:21], v[20:21], v[28:29]
	v_pk_mul_f32 v[22:23], v[22:23], v[30:31]
	v_lshl_add_u64 v[24:25], v[176:177], 0, s[16:17]
	global_store_dwordx4 v[24:25], v[20:23], off sc1
	s_nop 1
	v_pk_mul_f32 v[20:21], v[20:21], s[96:97] op_sel_hi:[1,0]
	v_pk_mul_f32 v[22:23], v[22:23], s[96:97] op_sel_hi:[1,0]
	v_exp_f32_e32 v16, v16
	v_exp_f32_e32 v17, v17
	v_exp_f32_e32 v18, v18
	v_pk_fma_f32 v[16:17], v[16:17], s[98:99], s[98:99] op_sel_hi:[1,0,0]
	v_exp_f32_e32 v19, v19
	v_exp_f32_e32 v20, v20
	v_pk_fma_f32 v[18:19], v[18:19], s[98:99], s[98:99] op_sel_hi:[1,0,0]
	v_exp_f32_e32 v21, v21
	v_exp_f32_e32 v22, v22
	v_pk_add_f32 v[20:21], v[20:21], 1.0 op_sel_hi:[1,0]
	v_exp_f32_e32 v23, v23
	v_pk_mul_f32 v[16:17], v[16:17], v[20:21]
	v_rcp_f32_e32 v16, v16
	v_pk_add_f32 v[22:23], v[22:23], 1.0 op_sel_hi:[1,0]
	v_rcp_f32_e32 v17, v17
	v_pk_mul_f32 v[18:19], v[18:19], v[22:23]
	v_pk_add_f32 v[20:21], v[20:21], 2.0 op_sel_hi:[1,0] neg_lo:[1,0] neg_hi:[1,0]
	v_rcp_f32_e32 v18, v18
	v_rcp_f32_e32 v19, v19
	v_pk_add_f32 v[22:23], v[22:23], 2.0 op_sel_hi:[1,0] neg_lo:[1,0] neg_hi:[1,0]
	v_pk_mul_f32 v[16:17], v[16:17], v[20:21]
	v_pk_mul_f32 v[18:19], v[18:19], v[22:23]
	v_cvt_pk_fp8_f32 v24, v16, v17
	v_or_b32_e32 v20, 32, v200
	v_ashrrev_i32_e32 v21, 31, v20
	v_lshlrev_b64 v[20:21], 10, v[20:21]
	v_cvt_pk_fp8_f32 v24, v18, v19 op_sel:[0,0,1]
	v_lshl_add_u64 v[22:23], v[122:123], 0, v[20:21]
	global_store_dword v[22:23], v24, off
	v_exp_f32_e32 v8, v8
	v_exp_f32_e32 v9, v9
	v_exp_f32_e32 v10, v10
	v_pk_add_f32 v[8:9], v[8:9], 1.0 op_sel_hi:[1,0]
	v_exp_f32_e32 v11, v11
	v_exp_f32_e32 v12, v12
	v_pk_add_f32 v[10:11], v[10:11], 1.0 op_sel_hi:[1,0]
	v_exp_f32_e32 v13, v13
	v_exp_f32_e32 v14, v14
	v_pk_add_f32 v[12:13], v[12:13], 1.0 op_sel_hi:[1,0]
	v_exp_f32_e32 v15, v15
	v_exp_f32_e32 v4, v4
	v_pk_add_f32 v[14:15], v[14:15], 1.0 op_sel_hi:[1,0]
	v_exp_f32_e32 v5, v5
	v_pk_mul_f32 v[8:9], v[8:9], v[12:13]
	v_exp_f32_e32 v6, v6
	v_pk_mul_f32 v[10:11], v[10:11], v[14:15]
	v_exp_f32_e32 v7, v7
	v_pk_add_f32 v[12:13], v[12:13], 2.0 op_sel_hi:[1,0] neg_lo:[1,0] neg_hi:[1,0]
	v_pk_add_f32 v[4:5], v[4:5], 1.0 op_sel_hi:[1,0]
	v_pk_add_f32 v[14:15], v[14:15], 2.0 op_sel_hi:[1,0] neg_lo:[1,0] neg_hi:[1,0]
	v_pk_add_f32 v[6:7], v[6:7], 1.0 op_sel_hi:[1,0]
	v_pk_mul_f32 v[12:13], v[12:13], v[4:5]
	v_pk_mul_f32 v[4:5], v[4:5], v[8:9]
	v_pk_mul_f32 v[14:15], v[14:15], v[6:7]
	v_pk_mul_f32 v[6:7], v[6:7], v[10:11]
	v_rcp_f32_e32 v4, v4
	v_rcp_f32_e32 v5, v5
	v_rcp_f32_e32 v6, v6
	v_rcp_f32_e32 v7, v7
	v_pk_fma_f32 v[12:13], v[144:145], v[8:9], v[12:13]
	v_pk_fma_f32 v[14:15], v[146:147], v[10:11], v[14:15]
	v_lshl_add_u64 v[8:9], v[176:177], 0, s[24:25]
	v_pk_mul_f32 v[4:5], v[4:5], v[12:13]
	v_pk_mul_f32 v[6:7], v[6:7], v[14:15]
	global_store_dwordx4 v[8:9], v[4:7], off sc1
	s_nop 1
	v_pk_mul_f32 v[4:5], v[4:5], s[96:97] op_sel_hi:[1,0]
	v_pk_mul_f32 v[6:7], v[6:7], s[96:97] op_sel_hi:[1,0]
	v_exp_f32_e32 v0, v0
	v_exp_f32_e32 v1, v1
	v_exp_f32_e32 v2, v2
	v_pk_fma_f32 v[0:1], v[0:1], s[98:99], s[98:99] op_sel_hi:[1,0,0]
	v_exp_f32_e32 v3, v3
	v_exp_f32_e32 v4, v4
	v_pk_fma_f32 v[2:3], v[2:3], s[98:99], s[98:99] op_sel_hi:[1,0,0]
	v_exp_f32_e32 v5, v5
	v_exp_f32_e32 v6, v6
	v_pk_add_f32 v[4:5], v[4:5], 1.0 op_sel_hi:[1,0]
	v_exp_f32_e32 v7, v7
	v_pk_mul_f32 v[0:1], v[0:1], v[4:5]
	v_rcp_f32_e32 v0, v0
	v_pk_add_f32 v[6:7], v[6:7], 1.0 op_sel_hi:[1,0]
	v_rcp_f32_e32 v1, v1
	v_pk_mul_f32 v[2:3], v[2:3], v[6:7]
	v_pk_add_f32 v[4:5], v[4:5], 2.0 op_sel_hi:[1,0] neg_lo:[1,0] neg_hi:[1,0]
	v_rcp_f32_e32 v2, v2
	v_rcp_f32_e32 v3, v3
	v_pk_add_f32 v[6:7], v[6:7], 2.0 op_sel_hi:[1,0] neg_lo:[1,0] neg_hi:[1,0]
	v_pk_mul_f32 v[0:1], v[0:1], v[4:5]
	v_pk_mul_f32 v[2:3], v[2:3], v[6:7]
	v_cvt_pk_fp8_f32 v8, v0, v1
	v_or_b32_e32 v4, 48, v200
	v_ashrrev_i32_e32 v5, 31, v4
	v_lshlrev_b64 v[4:5], 10, v[4:5]
	v_cvt_pk_fp8_f32 v8, v2, v3 op_sel:[0,0,1]
	v_lshl_add_u64 v[6:7], v[122:123], 0, v[4:5]
	global_store_dword v[6:7], v8, off
	s_branch .LBB2_24
.Lmy_epi_l7:
	v_exp_f32_e32 v120, v120
	v_exp_f32_e32 v121, v121
	v_exp_f32_e32 v122, v122
	v_pk_add_f32 v[120:121], v[120:121], 1.0 op_sel_hi:[1,0]
	v_exp_f32_e32 v123, v123
	v_exp_f32_e32 v124, v124
	v_pk_add_f32 v[122:123], v[122:123], 1.0 op_sel_hi:[1,0]
	v_exp_f32_e32 v125, v125
	v_exp_f32_e32 v126, v126
	v_pk_add_f32 v[124:125], v[124:125], 1.0 op_sel_hi:[1,0]
	v_exp_f32_e32 v127, v127
	v_exp_f32_e32 v116, v116
	v_pk_add_f32 v[126:127], v[126:127], 1.0 op_sel_hi:[1,0]
	v_exp_f32_e32 v117, v117
	v_pk_mul_f32 v[120:121], v[120:121], v[124:125]
	v_exp_f32_e32 v118, v118
	v_pk_mul_f32 v[122:123], v[122:123], v[126:127]
	v_exp_f32_e32 v119, v119
	v_pk_add_f32 v[124:125], v[124:125], 2.0 op_sel_hi:[1,0] neg_lo:[1,0] neg_hi:[1,0]
	v_pk_add_f32 v[116:117], v[116:117], 1.0 op_sel_hi:[1,0]
	v_pk_add_f32 v[126:127], v[126:127], 2.0 op_sel_hi:[1,0] neg_lo:[1,0] neg_hi:[1,0]
	v_pk_add_f32 v[118:119], v[118:119], 1.0 op_sel_hi:[1,0]
	v_pk_mul_f32 v[124:125], v[124:125], v[116:117]
	v_pk_mul_f32 v[116:117], v[116:117], v[120:121]
	v_pk_mul_f32 v[126:127], v[126:127], v[118:119]
	v_pk_mul_f32 v[118:119], v[118:119], v[122:123]
	v_rcp_f32_e32 v116, v116
	v_rcp_f32_e32 v117, v117
	v_rcp_f32_e32 v118, v118
	v_rcp_f32_e32 v119, v119
	s_waitcnt lgkmcnt(3)
	v_pk_fma_f32 v[124:125], v[172:173], v[120:121], v[124:125]
	v_pk_fma_f32 v[126:127], v[174:175], v[122:123], v[126:127]
	v_pk_mul_f32 v[116:117], v[116:117], v[124:125]
	v_pk_mul_f32 v[118:119], v[118:119], v[126:127]
	global_store_dwordx4 v[176:177], v[116:119], off sc1
	s_nop 1
	v_pk_mul_f32 v[116:117], v[116:117], s[96:97] op_sel_hi:[1,0]
	v_pk_mul_f32 v[118:119], v[118:119], s[96:97] op_sel_hi:[1,0]
	v_exp_f32_e32 v112, v112
	v_exp_f32_e32 v113, v113
	v_exp_f32_e32 v114, v114
	v_pk_fma_f32 v[112:113], v[112:113], s[98:99], s[98:99] op_sel_hi:[1,0,0]
	v_exp_f32_e32 v115, v115
	v_exp_f32_e32 v116, v116
	v_pk_fma_f32 v[114:115], v[114:115], s[98:99], s[98:99] op_sel_hi:[1,0,0]
	v_exp_f32_e32 v117, v117
	v_exp_f32_e32 v118, v118
	v_pk_add_f32 v[116:117], v[116:117], 1.0 op_sel_hi:[1,0]
	v_exp_f32_e32 v119, v119
	v_pk_mul_f32 v[112:113], v[112:113], v[116:117]
	v_rcp_f32_e32 v112, v112
	v_pk_add_f32 v[118:119], v[118:119], 1.0 op_sel_hi:[1,0]
	v_rcp_f32_e32 v113, v113
	v_pk_mul_f32 v[114:115], v[114:115], v[118:119]
	v_pk_add_f32 v[116:117], v[116:117], 2.0 op_sel_hi:[1,0] neg_lo:[1,0] neg_hi:[1,0]
	v_rcp_f32_e32 v114, v114
	v_rcp_f32_e32 v115, v115
	v_pk_add_f32 v[118:119], v[118:119], 2.0 op_sel_hi:[1,0] neg_lo:[1,0] neg_hi:[1,0]
	v_pk_mul_f32 v[112:113], v[112:113], v[116:117]
	v_pk_mul_f32 v[114:115], v[114:115], v[118:119]
	v_cvt_pk_fp8_f32 v124, v112, v113
	s_add_u32 s0, s8, s27
	s_addc_u32 s1, s9, 0
	s_ashr_i32 s35, s34, 31
	s_lshl_b64 s[34:35], s[34:35], 21
	v_ashrrev_i32_e32 v209, 31, v208
	s_add_u32 s36, s73, s34
	v_lshrrev_b32_e32 v126, 4, v210
	v_and_b32_e32 v127, 15, v210
	v_lshl_or_b32 v126, v126, 8, v127
	v_and_b32_e32 v127, 15, v208
	v_mul_u32_u24_e32 v127, 0x3f0, v127
	v_sub_u32_e32 v126, v126, v127
	v_ashrrev_i32_e32 v127, 31, v126
	v_lshl_add_u64 v[122:123], s[0:1], 0, v[126:127]
	v_cvt_pk_fp8_f32 v124, v114, v115 op_sel:[0,0,1]
	v_lshlrev_b64 v[116:117], 10, v[208:209]
	s_addc_u32 s37, s74, s35
	v_lshl_add_u64 v[118:119], v[122:123], 0, v[116:117]
	global_store_dword v[118:119], v124, off
	s_cmp_eq_u32 s30, 7
	s_cselect_b64 s[34:35], -1, 0
	s_cmp_lg_u32 s30, 7
	v_lshrrev_b32_e32 v126, 4, v210
	v_lshlrev_b32_e32 v126, 9, v126
	v_and_b32_e32 v127, 15, v210
	v_lshl_or_b32 v126, v127, 1, v126
	v_and_b32_e32 v127, 15, v208
	v_mul_u32_u24_e32 v127, 0x7e0, v127
	v_sub_u32_e32 v126, v126, v127
	v_ashrrev_i32_e32 v127, 31, v126
	v_lshl_add_u64 v[120:121], s[36:37], 0, v[126:127]
	v_pk_mul_f32 v[112:113], v[112:113], s[98:99] op_sel_hi:[1,0]
	v_pk_mul_f32 v[114:115], v[114:115], s[98:99] op_sel_hi:[1,0]
	v_cvt_pk_f16_f32 v112, v112, v113
	v_cvt_pk_f16_f32 v113, v114, v115
	v_lshl_add_u64 v[114:115], v[116:117], 1, v[120:121]
	global_store_dwordx2 v[114:115], v[112:113], off
	v_exp_f32_e32 v104, v104
	v_exp_f32_e32 v105, v105
	v_exp_f32_e32 v106, v106
	v_pk_add_f32 v[104:105], v[104:105], 1.0 op_sel_hi:[1,0]
	v_exp_f32_e32 v107, v107
	v_exp_f32_e32 v108, v108
	v_pk_add_f32 v[106:107], v[106:107], 1.0 op_sel_hi:[1,0]
	v_exp_f32_e32 v109, v109
	v_exp_f32_e32 v110, v110
	v_pk_add_f32 v[108:109], v[108:109], 1.0 op_sel_hi:[1,0]
	v_exp_f32_e32 v111, v111
	v_exp_f32_e32 v100, v100
	v_pk_add_f32 v[110:111], v[110:111], 1.0 op_sel_hi:[1,0]
	v_exp_f32_e32 v101, v101
	v_pk_mul_f32 v[104:105], v[104:105], v[108:109]
	v_exp_f32_e32 v102, v102
	v_pk_mul_f32 v[106:107], v[106:107], v[110:111]
	v_exp_f32_e32 v103, v103
	v_pk_add_f32 v[108:109], v[108:109], 2.0 op_sel_hi:[1,0] neg_lo:[1,0] neg_hi:[1,0]
	v_pk_add_f32 v[100:101], v[100:101], 1.0 op_sel_hi:[1,0]
	v_pk_add_f32 v[110:111], v[110:111], 2.0 op_sel_hi:[1,0] neg_lo:[1,0] neg_hi:[1,0]
	v_pk_add_f32 v[102:103], v[102:103], 1.0 op_sel_hi:[1,0]
	v_pk_mul_f32 v[108:109], v[108:109], v[100:101]
	v_pk_mul_f32 v[100:101], v[100:101], v[104:105]
	v_pk_mul_f32 v[110:111], v[110:111], v[102:103]
	v_pk_mul_f32 v[102:103], v[102:103], v[106:107]
	v_rcp_f32_e32 v100, v100
	v_rcp_f32_e32 v101, v101
	v_rcp_f32_e32 v102, v102
	v_rcp_f32_e32 v103, v103
	s_waitcnt lgkmcnt(2)
	v_pk_fma_f32 v[108:109], v[168:169], v[104:105], v[108:109]
	v_pk_fma_f32 v[110:111], v[170:171], v[106:107], v[110:111]
	v_lshl_add_u64 v[104:105], v[176:177], 0, s[18:19]
	v_pk_mul_f32 v[100:101], v[100:101], v[108:109]
	v_pk_mul_f32 v[102:103], v[102:103], v[110:111]
	global_store_dwordx4 v[104:105], v[100:103], off sc1
	s_nop 1
	v_pk_mul_f32 v[100:101], v[100:101], s[96:97] op_sel_hi:[1,0]
	v_pk_mul_f32 v[102:103], v[102:103], s[96:97] op_sel_hi:[1,0]
	v_exp_f32_e32 v96, v96
	v_exp_f32_e32 v97, v97
	v_exp_f32_e32 v98, v98
	v_pk_fma_f32 v[96:97], v[96:97], s[98:99], s[98:99] op_sel_hi:[1,0,0]
	v_exp_f32_e32 v99, v99
	v_exp_f32_e32 v100, v100
	v_pk_fma_f32 v[98:99], v[98:99], s[98:99], s[98:99] op_sel_hi:[1,0,0]
	v_exp_f32_e32 v101, v101
	v_exp_f32_e32 v102, v102
	v_pk_add_f32 v[100:101], v[100:101], 1.0 op_sel_hi:[1,0]
	v_exp_f32_e32 v103, v103
	v_pk_mul_f32 v[96:97], v[96:97], v[100:101]
	v_rcp_f32_e32 v96, v96
	v_pk_add_f32 v[102:103], v[102:103], 1.0 op_sel_hi:[1,0]
	v_rcp_f32_e32 v97, v97
	v_pk_mul_f32 v[98:99], v[98:99], v[102:103]
	v_pk_add_f32 v[100:101], v[100:101], 2.0 op_sel_hi:[1,0] neg_lo:[1,0] neg_hi:[1,0]
	v_rcp_f32_e32 v98, v98
	v_rcp_f32_e32 v99, v99
	v_pk_add_f32 v[102:103], v[102:103], 2.0 op_sel_hi:[1,0] neg_lo:[1,0] neg_hi:[1,0]
	v_pk_mul_f32 v[96:97], v[96:97], v[100:101]
	v_pk_mul_f32 v[98:99], v[98:99], v[102:103]
	v_cvt_pk_fp8_f32 v104, v96, v97
	v_ashrrev_i32_e32 v207, 31, v206
	v_lshlrev_b64 v[100:101], 10, v[206:207]
	v_lshl_add_u64 v[102:103], v[122:123], 0, v[100:101]
	v_cvt_pk_fp8_f32 v104, v98, v99 op_sel:[0,0,1]
	v_cndmask_b32_e64 v105, 0, 1, s[34:35]
	global_store_dword v[102:103], v104, off
	v_cmp_ne_u32_e64 s[0:1], 1, v105
	v_pk_mul_f32 v[96:97], v[96:97], s[98:99] op_sel_hi:[1,0]
	v_pk_mul_f32 v[98:99], v[98:99], s[98:99] op_sel_hi:[1,0]
	v_cvt_pk_f16_f32 v96, v96, v97
	v_cvt_pk_f16_f32 v97, v98, v99
	v_lshl_add_u64 v[98:99], v[100:101], 1, v[120:121]
	global_store_dwordx2 v[98:99], v[96:97], off
	v_exp_f32_e32 v88, v88
	v_exp_f32_e32 v89, v89
	v_exp_f32_e32 v90, v90
	v_pk_add_f32 v[88:89], v[88:89], 1.0 op_sel_hi:[1,0]
	v_exp_f32_e32 v91, v91
	v_exp_f32_e32 v92, v92
	v_pk_add_f32 v[90:91], v[90:91], 1.0 op_sel_hi:[1,0]
	v_exp_f32_e32 v93, v93
	v_exp_f32_e32 v94, v94
	v_pk_add_f32 v[92:93], v[92:93], 1.0 op_sel_hi:[1,0]
	v_exp_f32_e32 v95, v95
	v_exp_f32_e32 v84, v84
	v_pk_add_f32 v[94:95], v[94:95], 1.0 op_sel_hi:[1,0]
	v_exp_f32_e32 v85, v85
	v_pk_mul_f32 v[88:89], v[88:89], v[92:93]
	v_exp_f32_e32 v86, v86
	v_pk_mul_f32 v[90:91], v[90:91], v[94:95]
	v_exp_f32_e32 v87, v87
	v_pk_add_f32 v[92:93], v[92:93], 2.0 op_sel_hi:[1,0] neg_lo:[1,0] neg_hi:[1,0]
	v_pk_add_f32 v[84:85], v[84:85], 1.0 op_sel_hi:[1,0]
	v_pk_add_f32 v[94:95], v[94:95], 2.0 op_sel_hi:[1,0] neg_lo:[1,0] neg_hi:[1,0]
	v_pk_add_f32 v[86:87], v[86:87], 1.0 op_sel_hi:[1,0]
	v_pk_mul_f32 v[92:93], v[92:93], v[84:85]
	v_pk_mul_f32 v[84:85], v[84:85], v[88:89]
	v_pk_mul_f32 v[94:95], v[94:95], v[86:87]
	v_pk_mul_f32 v[86:87], v[86:87], v[90:91]
	v_rcp_f32_e32 v84, v84
	v_rcp_f32_e32 v85, v85
	v_rcp_f32_e32 v86, v86
	v_rcp_f32_e32 v87, v87
	s_waitcnt lgkmcnt(1)
	v_pk_fma_f32 v[92:93], v[164:165], v[88:89], v[92:93]
	v_pk_fma_f32 v[94:95], v[166:167], v[90:91], v[94:95]
	v_pk_mul_f32 v[84:85], v[84:85], v[92:93]
	v_pk_mul_f32 v[86:87], v[86:87], v[94:95]
	v_lshl_add_u64 v[88:89], v[176:177], 0, s[12:13]
	global_store_dwordx4 v[88:89], v[84:87], off sc1
	s_nop 1
	v_pk_mul_f32 v[84:85], v[84:85], s[96:97] op_sel_hi:[1,0]
	v_pk_mul_f32 v[86:87], v[86:87], s[96:97] op_sel_hi:[1,0]
	v_exp_f32_e32 v80, v80
	v_exp_f32_e32 v81, v81
	v_exp_f32_e32 v82, v82
	v_pk_fma_f32 v[80:81], v[80:81], s[98:99], s[98:99] op_sel_hi:[1,0,0]
	v_exp_f32_e32 v83, v83
	v_exp_f32_e32 v84, v84
	v_pk_fma_f32 v[82:83], v[82:83], s[98:99], s[98:99] op_sel_hi:[1,0,0]
	v_exp_f32_e32 v85, v85
	v_exp_f32_e32 v86, v86
	v_pk_add_f32 v[84:85], v[84:85], 1.0 op_sel_hi:[1,0]
	v_exp_f32_e32 v87, v87
	v_pk_mul_f32 v[80:81], v[80:81], v[84:85]
	v_rcp_f32_e32 v80, v80
	v_pk_add_f32 v[86:87], v[86:87], 1.0 op_sel_hi:[1,0]
	v_rcp_f32_e32 v81, v81
	v_pk_mul_f32 v[82:83], v[82:83], v[86:87]
	v_pk_add_f32 v[84:85], v[84:85], 2.0 op_sel_hi:[1,0] neg_lo:[1,0] neg_hi:[1,0]
	v_rcp_f32_e32 v82, v82
	v_rcp_f32_e32 v83, v83
	v_pk_add_f32 v[86:87], v[86:87], 2.0 op_sel_hi:[1,0] neg_lo:[1,0] neg_hi:[1,0]
	v_pk_mul_f32 v[80:81], v[80:81], v[84:85]
	v_pk_mul_f32 v[82:83], v[82:83], v[86:87]
	v_ashrrev_i32_e32 v205, 31, v204
	v_cvt_pk_fp8_f32 v88, v80, v81
	s_and_b64 vcc, exec, s[0:1]
	v_cvt_pk_fp8_f32 v88, v82, v83 op_sel:[0,0,1]
	v_lshlrev_b64 v[84:85], 10, v[204:205]
	v_lshl_add_u64 v[86:87], v[122:123], 0, v[84:85]
	global_store_dword v[86:87], v88, off
	v_pk_mul_f32 v[80:81], v[80:81], s[98:99] op_sel_hi:[1,0]
	v_pk_mul_f32 v[82:83], v[82:83], s[98:99] op_sel_hi:[1,0]
	v_cvt_pk_f16_f32 v80, v80, v81
	v_cvt_pk_f16_f32 v81, v82, v83
	v_lshl_add_u64 v[82:83], v[84:85], 1, v[120:121]
	global_store_dwordx2 v[82:83], v[80:81], off
	v_exp_f32_e32 v72, v72
	v_exp_f32_e32 v73, v73
	v_exp_f32_e32 v74, v74
	v_pk_add_f32 v[72:73], v[72:73], 1.0 op_sel_hi:[1,0]
	v_exp_f32_e32 v75, v75
	v_exp_f32_e32 v76, v76
	v_pk_add_f32 v[74:75], v[74:75], 1.0 op_sel_hi:[1,0]
	v_exp_f32_e32 v77, v77
	v_exp_f32_e32 v78, v78
	v_pk_add_f32 v[76:77], v[76:77], 1.0 op_sel_hi:[1,0]
	v_exp_f32_e32 v79, v79
	v_exp_f32_e32 v68, v68
	v_pk_add_f32 v[78:79], v[78:79], 1.0 op_sel_hi:[1,0]
	v_exp_f32_e32 v69, v69
	v_pk_mul_f32 v[72:73], v[72:73], v[76:77]
	v_exp_f32_e32 v70, v70
	v_pk_mul_f32 v[74:75], v[74:75], v[78:79]
	v_exp_f32_e32 v71, v71
	v_pk_add_f32 v[76:77], v[76:77], 2.0 op_sel_hi:[1,0] neg_lo:[1,0] neg_hi:[1,0]
	v_pk_add_f32 v[68:69], v[68:69], 1.0 op_sel_hi:[1,0]
	v_pk_add_f32 v[78:79], v[78:79], 2.0 op_sel_hi:[1,0] neg_lo:[1,0] neg_hi:[1,0]
	v_pk_add_f32 v[70:71], v[70:71], 1.0 op_sel_hi:[1,0]
	v_pk_mul_f32 v[76:77], v[76:77], v[68:69]
	v_pk_mul_f32 v[68:69], v[68:69], v[72:73]
	v_pk_mul_f32 v[78:79], v[78:79], v[70:71]
	v_pk_mul_f32 v[70:71], v[70:71], v[74:75]
	v_rcp_f32_e32 v68, v68
	v_rcp_f32_e32 v69, v69
	v_rcp_f32_e32 v70, v70
	v_rcp_f32_e32 v71, v71
	s_waitcnt lgkmcnt(0)
	v_pk_fma_f32 v[76:77], v[160:161], v[72:73], v[76:77]
	v_pk_fma_f32 v[78:79], v[162:163], v[74:75], v[78:79]
	v_lshl_add_u64 v[72:73], v[176:177], 0, s[20:21]
	v_pk_mul_f32 v[68:69], v[68:69], v[76:77]
	v_pk_mul_f32 v[70:71], v[70:71], v[78:79]
	global_store_dwordx4 v[72:73], v[68:71], off sc1
	s_nop 1
	v_pk_mul_f32 v[68:69], v[68:69], s[96:97] op_sel_hi:[1,0]
	v_pk_mul_f32 v[70:71], v[70:71], s[96:97] op_sel_hi:[1,0]
	v_exp_f32_e32 v64, v64
	v_exp_f32_e32 v65, v65
	v_exp_f32_e32 v66, v66
	v_pk_fma_f32 v[64:65], v[64:65], s[98:99], s[98:99] op_sel_hi:[1,0,0]
	v_exp_f32_e32 v67, v67
	v_exp_f32_e32 v68, v68
	v_pk_fma_f32 v[66:67], v[66:67], s[98:99], s[98:99] op_sel_hi:[1,0,0]
	v_exp_f32_e32 v69, v69
	v_exp_f32_e32 v70, v70
	v_pk_add_f32 v[68:69], v[68:69], 1.0 op_sel_hi:[1,0]
	v_exp_f32_e32 v71, v71
	v_pk_mul_f32 v[64:65], v[64:65], v[68:69]
	v_rcp_f32_e32 v64, v64
	v_pk_add_f32 v[70:71], v[70:71], 1.0 op_sel_hi:[1,0]
	v_rcp_f32_e32 v65, v65
	v_pk_mul_f32 v[66:67], v[66:67], v[70:71]
	v_pk_add_f32 v[68:69], v[68:69], 2.0 op_sel_hi:[1,0] neg_lo:[1,0] neg_hi:[1,0]
	v_rcp_f32_e32 v66, v66
	v_rcp_f32_e32 v67, v67
	v_pk_add_f32 v[70:71], v[70:71], 2.0 op_sel_hi:[1,0] neg_lo:[1,0] neg_hi:[1,0]
	v_pk_mul_f32 v[64:65], v[64:65], v[68:69]
	v_pk_mul_f32 v[66:67], v[66:67], v[70:71]
	v_ashrrev_i32_e32 v203, 31, v202
	v_cvt_pk_fp8_f32 v72, v64, v65
	s_and_b64 vcc, exec, s[0:1]
	v_cvt_pk_fp8_f32 v72, v66, v67 op_sel:[0,0,1]
	v_lshlrev_b64 v[68:69], 10, v[202:203]
	v_lshl_add_u64 v[70:71], v[122:123], 0, v[68:69]
	global_store_dword v[70:71], v72, off
	v_pk_mul_f32 v[64:65], v[64:65], s[98:99] op_sel_hi:[1,0]
	v_pk_mul_f32 v[66:67], v[66:67], s[98:99] op_sel_hi:[1,0]
	v_cvt_pk_f16_f32 v64, v64, v65
	v_cvt_pk_f16_f32 v65, v66, v67
	v_lshl_add_u64 v[66:67], v[68:69], 1, v[120:121]
	global_store_dwordx2 v[66:67], v[64:65], off
	v_exp_f32_e32 v56, v56
	v_exp_f32_e32 v57, v57
	v_exp_f32_e32 v58, v58
	v_pk_add_f32 v[56:57], v[56:57], 1.0 op_sel_hi:[1,0]
	v_exp_f32_e32 v59, v59
	v_exp_f32_e32 v60, v60
	v_pk_add_f32 v[58:59], v[58:59], 1.0 op_sel_hi:[1,0]
	v_exp_f32_e32 v61, v61
	v_exp_f32_e32 v62, v62
	v_pk_add_f32 v[60:61], v[60:61], 1.0 op_sel_hi:[1,0]
	v_exp_f32_e32 v63, v63
	v_exp_f32_e32 v52, v52
	v_pk_add_f32 v[62:63], v[62:63], 1.0 op_sel_hi:[1,0]
	v_exp_f32_e32 v53, v53
	v_pk_mul_f32 v[56:57], v[56:57], v[60:61]
	v_exp_f32_e32 v54, v54
	v_pk_mul_f32 v[58:59], v[58:59], v[62:63]
	v_exp_f32_e32 v55, v55
	v_pk_add_f32 v[60:61], v[60:61], 2.0 op_sel_hi:[1,0] neg_lo:[1,0] neg_hi:[1,0]
	v_pk_add_f32 v[52:53], v[52:53], 1.0 op_sel_hi:[1,0]
	v_pk_add_f32 v[62:63], v[62:63], 2.0 op_sel_hi:[1,0] neg_lo:[1,0] neg_hi:[1,0]
	v_pk_add_f32 v[54:55], v[54:55], 1.0 op_sel_hi:[1,0]
	v_pk_mul_f32 v[60:61], v[60:61], v[52:53]
	v_pk_mul_f32 v[52:53], v[52:53], v[56:57]
	v_pk_mul_f32 v[62:63], v[62:63], v[54:55]
	v_pk_mul_f32 v[54:55], v[54:55], v[58:59]
	v_rcp_f32_e32 v52, v52
	v_rcp_f32_e32 v53, v53
	v_rcp_f32_e32 v54, v54
	v_rcp_f32_e32 v55, v55
	s_waitcnt vmcnt(8)
	v_pk_fma_f32 v[60:61], v[156:157], v[56:57], v[60:61]
	v_pk_fma_f32 v[62:63], v[158:159], v[58:59], v[62:63]
	v_pk_mul_f32 v[52:53], v[52:53], v[60:61]
	v_pk_mul_f32 v[54:55], v[54:55], v[62:63]
	v_lshl_add_u64 v[56:57], v[176:177], 0, s[14:15]
	global_store_dwordx4 v[56:57], v[52:55], off sc1
	s_nop 1
	v_pk_mul_f32 v[52:53], v[52:53], s[96:97] op_sel_hi:[1,0]
	v_pk_mul_f32 v[54:55], v[54:55], s[96:97] op_sel_hi:[1,0]
	v_exp_f32_e32 v48, v48
	v_exp_f32_e32 v49, v49
	v_exp_f32_e32 v50, v50
	v_pk_fma_f32 v[48:49], v[48:49], s[98:99], s[98:99] op_sel_hi:[1,0,0]
	v_exp_f32_e32 v51, v51
	v_exp_f32_e32 v52, v52
	v_pk_fma_f32 v[50:51], v[50:51], s[98:99], s[98:99] op_sel_hi:[1,0,0]
	v_exp_f32_e32 v53, v53
	v_exp_f32_e32 v54, v54
	v_pk_add_f32 v[52:53], v[52:53], 1.0 op_sel_hi:[1,0]
	v_exp_f32_e32 v55, v55
	v_pk_mul_f32 v[48:49], v[48:49], v[52:53]
	v_rcp_f32_e32 v48, v48
	v_pk_add_f32 v[54:55], v[54:55], 1.0 op_sel_hi:[1,0]
	v_rcp_f32_e32 v49, v49
	v_pk_mul_f32 v[50:51], v[50:51], v[54:55]
	v_pk_add_f32 v[52:53], v[52:53], 2.0 op_sel_hi:[1,0] neg_lo:[1,0] neg_hi:[1,0]
	v_rcp_f32_e32 v50, v50
	v_rcp_f32_e32 v51, v51
	v_pk_add_f32 v[54:55], v[54:55], 2.0 op_sel_hi:[1,0] neg_lo:[1,0] neg_hi:[1,0]
	v_pk_mul_f32 v[48:49], v[48:49], v[52:53]
	v_pk_mul_f32 v[50:51], v[50:51], v[54:55]
	v_ashrrev_i32_e32 v201, 31, v200
	v_cvt_pk_fp8_f32 v56, v48, v49
	s_and_b64 vcc, exec, s[0:1]
	v_cvt_pk_fp8_f32 v56, v50, v51 op_sel:[0,0,1]
	v_lshlrev_b64 v[52:53], 10, v[200:201]
	v_lshl_add_u64 v[54:55], v[122:123], 0, v[52:53]
	global_store_dword v[54:55], v56, off
	v_pk_mul_f32 v[48:49], v[48:49], s[98:99] op_sel_hi:[1,0]
	v_pk_mul_f32 v[50:51], v[50:51], s[98:99] op_sel_hi:[1,0]
	v_cvt_pk_f16_f32 v48, v48, v49
	v_cvt_pk_f16_f32 v49, v50, v51
	v_lshl_add_u64 v[50:51], v[52:53], 1, v[120:121]
	global_store_dwordx2 v[50:51], v[48:49], off
	v_exp_f32_e32 v40, v40
	v_exp_f32_e32 v41, v41
	v_exp_f32_e32 v42, v42
	v_pk_add_f32 v[40:41], v[40:41], 1.0 op_sel_hi:[1,0]
	v_exp_f32_e32 v43, v43
	v_exp_f32_e32 v44, v44
	v_pk_add_f32 v[42:43], v[42:43], 1.0 op_sel_hi:[1,0]
	v_exp_f32_e32 v45, v45
	v_exp_f32_e32 v46, v46
	v_pk_add_f32 v[44:45], v[44:45], 1.0 op_sel_hi:[1,0]
	v_exp_f32_e32 v47, v47
	v_exp_f32_e32 v36, v36
	v_pk_add_f32 v[46:47], v[46:47], 1.0 op_sel_hi:[1,0]
	v_exp_f32_e32 v37, v37
	v_pk_mul_f32 v[40:41], v[40:41], v[44:45]
	v_exp_f32_e32 v38, v38
	v_pk_mul_f32 v[42:43], v[42:43], v[46:47]
	v_exp_f32_e32 v39, v39
	v_pk_add_f32 v[44:45], v[44:45], 2.0 op_sel_hi:[1,0] neg_lo:[1,0] neg_hi:[1,0]
	v_pk_add_f32 v[36:37], v[36:37], 1.0 op_sel_hi:[1,0]
	v_pk_add_f32 v[46:47], v[46:47], 2.0 op_sel_hi:[1,0] neg_lo:[1,0] neg_hi:[1,0]
	v_pk_add_f32 v[38:39], v[38:39], 1.0 op_sel_hi:[1,0]
	v_pk_mul_f32 v[44:45], v[44:45], v[36:37]
	v_pk_mul_f32 v[36:37], v[36:37], v[40:41]
	v_pk_mul_f32 v[46:47], v[46:47], v[38:39]
	v_pk_mul_f32 v[38:39], v[38:39], v[42:43]
	v_rcp_f32_e32 v36, v36
	v_rcp_f32_e32 v37, v37
	v_rcp_f32_e32 v38, v38
	v_rcp_f32_e32 v39, v39
	v_pk_fma_f32 v[44:45], v[152:153], v[40:41], v[44:45]
	v_pk_fma_f32 v[46:47], v[154:155], v[42:43], v[46:47]
	v_lshl_add_u64 v[40:41], v[176:177], 0, s[22:23]
	v_pk_mul_f32 v[36:37], v[36:37], v[44:45]
	v_pk_mul_f32 v[38:39], v[38:39], v[46:47]
	global_store_dwordx4 v[40:41], v[36:39], off sc1
	s_nop 1
	v_pk_mul_f32 v[36:37], v[36:37], s[96:97] op_sel_hi:[1,0]
	v_pk_mul_f32 v[38:39], v[38:39], s[96:97] op_sel_hi:[1,0]
	v_exp_f32_e32 v32, v32
	v_exp_f32_e32 v33, v33
	v_exp_f32_e32 v34, v34
	v_pk_fma_f32 v[32:33], v[32:33], s[98:99], s[98:99] op_sel_hi:[1,0,0]
	v_exp_f32_e32 v35, v35
	v_exp_f32_e32 v36, v36
	v_pk_fma_f32 v[34:35], v[34:35], s[98:99], s[98:99] op_sel_hi:[1,0,0]
	v_exp_f32_e32 v37, v37
	v_exp_f32_e32 v38, v38
	v_pk_add_f32 v[36:37], v[36:37], 1.0 op_sel_hi:[1,0]
	v_exp_f32_e32 v39, v39
	v_pk_mul_f32 v[32:33], v[32:33], v[36:37]
	v_rcp_f32_e32 v32, v32
	v_pk_add_f32 v[38:39], v[38:39], 1.0 op_sel_hi:[1,0]
	v_rcp_f32_e32 v33, v33
	v_pk_mul_f32 v[34:35], v[34:35], v[38:39]
	v_pk_add_f32 v[36:37], v[36:37], 2.0 op_sel_hi:[1,0] neg_lo:[1,0] neg_hi:[1,0]
	v_rcp_f32_e32 v34, v34
	v_rcp_f32_e32 v35, v35
	v_pk_add_f32 v[38:39], v[38:39], 2.0 op_sel_hi:[1,0] neg_lo:[1,0] neg_hi:[1,0]
	v_pk_mul_f32 v[32:33], v[32:33], v[36:37]
	v_pk_mul_f32 v[34:35], v[34:35], v[38:39]
	v_cvt_pk_fp8_f32 v40, v32, v33
	v_or_b32_e32 v36, 16, v200
	v_ashrrev_i32_e32 v37, 31, v36
	v_lshlrev_b64 v[36:37], 10, v[36:37]
	v_cvt_pk_fp8_f32 v40, v34, v35 op_sel:[0,0,1]
	v_lshl_add_u64 v[38:39], v[122:123], 0, v[36:37]
	global_store_dword v[38:39], v40, off
	v_pk_mul_f32 v[32:33], v[32:33], s[98:99] op_sel_hi:[1,0]
	v_pk_mul_f32 v[34:35], v[34:35], s[98:99] op_sel_hi:[1,0]
	v_cvt_pk_f16_f32 v32, v32, v33
	v_cvt_pk_f16_f32 v33, v34, v35
	v_lshl_add_u64 v[34:35], v[36:37], 1, v[120:121]
	global_store_dwordx2 v[34:35], v[32:33], off
	v_exp_f32_e32 v24, v24
	v_exp_f32_e32 v25, v25
	v_exp_f32_e32 v26, v26
	v_pk_add_f32 v[24:25], v[24:25], 1.0 op_sel_hi:[1,0]
	v_exp_f32_e32 v27, v27
	v_exp_f32_e32 v28, v28
	v_pk_add_f32 v[26:27], v[26:27], 1.0 op_sel_hi:[1,0]
	v_exp_f32_e32 v29, v29
	v_exp_f32_e32 v30, v30
	v_pk_add_f32 v[28:29], v[28:29], 1.0 op_sel_hi:[1,0]
	v_exp_f32_e32 v31, v31
	v_exp_f32_e32 v20, v20
	v_pk_add_f32 v[30:31], v[30:31], 1.0 op_sel_hi:[1,0]
	v_exp_f32_e32 v21, v21
	v_pk_mul_f32 v[24:25], v[24:25], v[28:29]
	v_exp_f32_e32 v22, v22
	v_pk_mul_f32 v[26:27], v[26:27], v[30:31]
	v_exp_f32_e32 v23, v23
	v_pk_add_f32 v[28:29], v[28:29], 2.0 op_sel_hi:[1,0] neg_lo:[1,0] neg_hi:[1,0]
	v_pk_add_f32 v[20:21], v[20:21], 1.0 op_sel_hi:[1,0]
	v_pk_add_f32 v[30:31], v[30:31], 2.0 op_sel_hi:[1,0] neg_lo:[1,0] neg_hi:[1,0]
	v_pk_add_f32 v[22:23], v[22:23], 1.0 op_sel_hi:[1,0]
	v_pk_mul_f32 v[28:29], v[28:29], v[20:21]
	v_pk_mul_f32 v[20:21], v[20:21], v[24:25]
	v_pk_mul_f32 v[30:31], v[30:31], v[22:23]
	v_pk_mul_f32 v[22:23], v[22:23], v[26:27]
	v_rcp_f32_e32 v20, v20
	v_rcp_f32_e32 v21, v21
	v_rcp_f32_e32 v22, v22
	v_rcp_f32_e32 v23, v23
	v_pk_fma_f32 v[28:29], v[148:149], v[24:25], v[28:29]
	v_pk_fma_f32 v[30:31], v[150:151], v[26:27], v[30:31]
	v_pk_mul_f32 v[20:21], v[20:21], v[28:29]
	v_pk_mul_f32 v[22:23], v[22:23], v[30:31]
	v_lshl_add_u64 v[24:25], v[176:177], 0, s[16:17]
	global_store_dwordx4 v[24:25], v[20:23], off sc1
	s_nop 1
	v_pk_mul_f32 v[20:21], v[20:21], s[96:97] op_sel_hi:[1,0]
	v_pk_mul_f32 v[22:23], v[22:23], s[96:97] op_sel_hi:[1,0]
	v_exp_f32_e32 v16, v16
	v_exp_f32_e32 v17, v17
	v_exp_f32_e32 v18, v18
	v_pk_fma_f32 v[16:17], v[16:17], s[98:99], s[98:99] op_sel_hi:[1,0,0]
	v_exp_f32_e32 v19, v19
	v_exp_f32_e32 v20, v20
	v_pk_fma_f32 v[18:19], v[18:19], s[98:99], s[98:99] op_sel_hi:[1,0,0]
	v_exp_f32_e32 v21, v21
	v_exp_f32_e32 v22, v22
	v_pk_add_f32 v[20:21], v[20:21], 1.0 op_sel_hi:[1,0]
	v_exp_f32_e32 v23, v23
	v_pk_mul_f32 v[16:17], v[16:17], v[20:21]
	v_rcp_f32_e32 v16, v16
	v_pk_add_f32 v[22:23], v[22:23], 1.0 op_sel_hi:[1,0]
	v_rcp_f32_e32 v17, v17
	v_pk_mul_f32 v[18:19], v[18:19], v[22:23]
	v_pk_add_f32 v[20:21], v[20:21], 2.0 op_sel_hi:[1,0] neg_lo:[1,0] neg_hi:[1,0]
	v_rcp_f32_e32 v18, v18
	v_rcp_f32_e32 v19, v19
	v_pk_add_f32 v[22:23], v[22:23], 2.0 op_sel_hi:[1,0] neg_lo:[1,0] neg_hi:[1,0]
	v_pk_mul_f32 v[16:17], v[16:17], v[20:21]
	v_pk_mul_f32 v[18:19], v[18:19], v[22:23]
	v_cvt_pk_fp8_f32 v24, v16, v17
	v_or_b32_e32 v20, 32, v200
	v_ashrrev_i32_e32 v21, 31, v20
	v_lshlrev_b64 v[20:21], 10, v[20:21]
	v_cvt_pk_fp8_f32 v24, v18, v19 op_sel:[0,0,1]
	v_lshl_add_u64 v[22:23], v[122:123], 0, v[20:21]
	global_store_dword v[22:23], v24, off
	v_pk_mul_f32 v[16:17], v[16:17], s[98:99] op_sel_hi:[1,0]
	v_pk_mul_f32 v[18:19], v[18:19], s[98:99] op_sel_hi:[1,0]
	v_cvt_pk_f16_f32 v16, v16, v17
	v_cvt_pk_f16_f32 v17, v18, v19
	v_lshl_add_u64 v[18:19], v[20:21], 1, v[120:121]
	global_store_dwordx2 v[18:19], v[16:17], off
	v_exp_f32_e32 v8, v8
	v_exp_f32_e32 v9, v9
	v_exp_f32_e32 v10, v10
	v_pk_add_f32 v[8:9], v[8:9], 1.0 op_sel_hi:[1,0]
	v_exp_f32_e32 v11, v11
	v_exp_f32_e32 v12, v12
	v_pk_add_f32 v[10:11], v[10:11], 1.0 op_sel_hi:[1,0]
	v_exp_f32_e32 v13, v13
	v_exp_f32_e32 v14, v14
	v_pk_add_f32 v[12:13], v[12:13], 1.0 op_sel_hi:[1,0]
	v_exp_f32_e32 v15, v15
	v_exp_f32_e32 v4, v4
	v_pk_add_f32 v[14:15], v[14:15], 1.0 op_sel_hi:[1,0]
	v_exp_f32_e32 v5, v5
	v_pk_mul_f32 v[8:9], v[8:9], v[12:13]
	v_exp_f32_e32 v6, v6
	v_pk_mul_f32 v[10:11], v[10:11], v[14:15]
	v_exp_f32_e32 v7, v7
	v_pk_add_f32 v[12:13], v[12:13], 2.0 op_sel_hi:[1,0] neg_lo:[1,0] neg_hi:[1,0]
	v_pk_add_f32 v[4:5], v[4:5], 1.0 op_sel_hi:[1,0]
	v_pk_add_f32 v[14:15], v[14:15], 2.0 op_sel_hi:[1,0] neg_lo:[1,0] neg_hi:[1,0]
	v_pk_add_f32 v[6:7], v[6:7], 1.0 op_sel_hi:[1,0]
	v_pk_mul_f32 v[12:13], v[12:13], v[4:5]
	v_pk_mul_f32 v[4:5], v[4:5], v[8:9]
	v_pk_mul_f32 v[14:15], v[14:15], v[6:7]
	v_pk_mul_f32 v[6:7], v[6:7], v[10:11]
	v_rcp_f32_e32 v4, v4
	v_rcp_f32_e32 v5, v5
	v_rcp_f32_e32 v6, v6
	v_rcp_f32_e32 v7, v7
	v_pk_fma_f32 v[12:13], v[144:145], v[8:9], v[12:13]
	v_pk_fma_f32 v[14:15], v[146:147], v[10:11], v[14:15]
	v_lshl_add_u64 v[8:9], v[176:177], 0, s[24:25]
	v_pk_mul_f32 v[4:5], v[4:5], v[12:13]
	v_pk_mul_f32 v[6:7], v[6:7], v[14:15]
	global_store_dwordx4 v[8:9], v[4:7], off sc1
	s_nop 1
	v_pk_mul_f32 v[4:5], v[4:5], s[96:97] op_sel_hi:[1,0]
	v_pk_mul_f32 v[6:7], v[6:7], s[96:97] op_sel_hi:[1,0]
	v_exp_f32_e32 v0, v0
	v_exp_f32_e32 v1, v1
	v_exp_f32_e32 v2, v2
	v_pk_fma_f32 v[0:1], v[0:1], s[98:99], s[98:99] op_sel_hi:[1,0,0]
	v_exp_f32_e32 v3, v3
	v_exp_f32_e32 v4, v4
	v_pk_fma_f32 v[2:3], v[2:3], s[98:99], s[98:99] op_sel_hi:[1,0,0]
	v_exp_f32_e32 v5, v5
	v_exp_f32_e32 v6, v6
	v_pk_add_f32 v[4:5], v[4:5], 1.0 op_sel_hi:[1,0]
	v_exp_f32_e32 v7, v7
	v_pk_mul_f32 v[0:1], v[0:1], v[4:5]
	v_rcp_f32_e32 v0, v0
	v_pk_add_f32 v[6:7], v[6:7], 1.0 op_sel_hi:[1,0]
	v_rcp_f32_e32 v1, v1
	v_pk_mul_f32 v[2:3], v[2:3], v[6:7]
	v_pk_add_f32 v[4:5], v[4:5], 2.0 op_sel_hi:[1,0] neg_lo:[1,0] neg_hi:[1,0]
	v_rcp_f32_e32 v2, v2
	v_rcp_f32_e32 v3, v3
	v_pk_add_f32 v[6:7], v[6:7], 2.0 op_sel_hi:[1,0] neg_lo:[1,0] neg_hi:[1,0]
	v_pk_mul_f32 v[0:1], v[0:1], v[4:5]
	v_pk_mul_f32 v[2:3], v[2:3], v[6:7]
	v_cvt_pk_fp8_f32 v8, v0, v1
	v_or_b32_e32 v4, 48, v200
	v_ashrrev_i32_e32 v5, 31, v4
	v_lshlrev_b64 v[4:5], 10, v[4:5]
	v_cvt_pk_fp8_f32 v8, v2, v3 op_sel:[0,0,1]
	v_lshl_add_u64 v[6:7], v[122:123], 0, v[4:5]
	global_store_dword v[6:7], v8, off
	v_pk_mul_f32 v[0:1], v[0:1], s[98:99] op_sel_hi:[1,0]
	v_pk_mul_f32 v[2:3], v[2:3], s[98:99] op_sel_hi:[1,0]
	v_cvt_pk_f16_f32 v0, v0, v1
	v_cvt_pk_f16_f32 v1, v2, v3
	v_lshl_add_u64 v[2:3], v[4:5], 1, v[120:121]
	global_store_dwordx2 v[2:3], v[0:1], off
	s_branch .LBB2_24

_Z11dec_in_projPKDF16_PKfS2_Pf:
	v_lshl_or_b32 v1, s2, 8, v0
	s_mov_b32 s2, 0x1c000
	v_cmp_gt_u32_e32 vcc, s2, v1
	s_and_saveexec_b64 s[2:3], vcc
	s_cbranch_execz .LBB3_4
	s_load_dwordx8 s[4:11], s[0:1], 0x0
	v_lshrrev_b32_e32 v1, 2, v1
	v_and_b32_e32 v1, 0x3ffffff0, v1
	v_and_b32_e32 v2, 15, v0
	v_lshlrev_b32_e32 v4, 1, v0
	v_or_b32_e32 v3, v1, v2
	v_and_b32_e32 v4, 0x60, v4
	v_mov_b32_e32 v7, 0
	v_lshl_or_b32 v6, v2, 12, v4
	v_lshlrev_b32_e32 v3, 11, v1
	s_waitcnt lgkmcnt(0)
	v_lshl_add_u64 v[4:5], s[6:7], 0, v[6:7]
	s_mov_b64 s[0:1], 0x190
	v_lshl_or_b32 v3, v2, 5, v3
	v_and_or_b32 v3, v0, 16, v3
	v_and_b32_e32 v6, 32, v0
	v_lshl_or_b32 v6, v6, 4, v3
	v_lshl_add_u64 v[4:5], v[4:5], 0, s[0:1]
	v_lshl_add_u64 v[6:7], s[4:5], 0, v[6:7]
	s_mov_b64 s[0:1], 0x800
	v_accvgpr_write_b32 a3, 0
	v_accvgpr_write_b32 a2, 0
	v_accvgpr_write_b32 a1, 0
	v_accvgpr_write_b32 a0, 0
	v_lshl_add_u64 v[6:7], v[6:7], 0, s[0:1]
	s_movk_i32 s4, 0xffe0
	s_mov_b64 s[0:1], 0x200
	s_mov_b64 s[2:3], 0x1000
.LBB3_2:
	global_load_dwordx4 v[8:11], v[6:7], off offset:-2048
	global_load_dwordx4 v[12:15], v[4:5], off offset:-384
	global_load_dwordx4 v[16:19], v[4:5], off offset:-400
	s_addk_i32 s4, 0x80
	s_cmpk_gt_u32 s4, 0x3df
	s_waitcnt vmcnt(1)
	v_cvt_pk_f16_f32 v22, v12, v13
	s_waitcnt vmcnt(0)
	v_cvt_f16_f32_e32 v3, v16
	v_cvt_f16_f32_e32 v21, v17
	v_cvt_pk_f16_f32 v20, v16, v17
	v_cvt_pk_f16_f32 v23, v14, v15
	v_cvt_f32_f16_e32 v3, v3
	v_sub_f32_e32 v3, v16, v3
	v_cvt_f32_f16_e32 v16, v21
	v_cvt_pk_f16_f32 v21, v18, v19
	v_sub_f32_e32 v16, v17, v16
	v_cvt_pk_f16_f32 v24, v3, v16
	v_cvt_f32_f16_e32 v16, v22
	v_cvt_f32_f16_sdwa v17, v22 dst_sel:DWORD dst_unused:UNUSED_PAD src0_sel:WORD_1
	v_mfma_f32_16x16x32_f16 a[0:3], v[8:11], v[20:23], a[0:3]
	v_add_f32_e64 v12, v12, -v16
	v_add_f32_e64 v13, v13, -v17
	v_cvt_pk_f16_f32 v26, v12, v13
	v_cvt_f32_f16_e32 v12, v21
	v_cvt_f32_f16_sdwa v13, v21 dst_sel:DWORD dst_unused:UNUSED_PAD src0_sel:WORD_1
	v_pk_add_f32 v[12:13], v[18:19], v[12:13] neg_lo:[0,1] neg_hi:[0,1]
	s_nop 0
	v_cvt_pk_f16_f32 v25, v12, v13
	v_cvt_f32_f16_e32 v12, v23
	v_cvt_f32_f16_sdwa v13, v23 dst_sel:DWORD dst_unused:UNUSED_PAD src0_sel:WORD_1
	v_pk_add_f32 v[12:13], v[14:15], v[12:13] neg_lo:[0,1] neg_hi:[0,1]
	s_nop 0
	v_cvt_pk_f16_f32 v27, v12, v13
	s_nop 1
	v_mfma_f32_16x16x32_f16 a[0:3], v[8:11], v[24:27], a[0:3]
	global_load_dwordx4 v[8:11], v[6:7], off offset:-1024
	global_load_dwordx4 v[12:15], v[4:5], off offset:-256
	global_load_dwordx4 v[16:19], v[4:5], off offset:-272
	s_waitcnt vmcnt(1)
	v_cvt_pk_f16_f32 v22, v12, v13
	s_waitcnt vmcnt(0)
	v_cvt_f16_f32_e32 v3, v16
	v_cvt_f16_f32_e32 v21, v17
	v_cvt_pk_f16_f32 v20, v16, v17
	v_cvt_pk_f16_f32 v23, v14, v15
	v_cvt_f32_f16_e32 v3, v3
	v_sub_f32_e32 v3, v16, v3
	v_cvt_f32_f16_e32 v16, v21
	v_cvt_pk_f16_f32 v21, v18, v19
	v_sub_f32_e32 v16, v17, v16
	v_cvt_pk_f16_f32 v24, v3, v16
	v_cvt_f32_f16_e32 v16, v22
	v_cvt_f32_f16_sdwa v17, v22 dst_sel:DWORD dst_unused:UNUSED_PAD src0_sel:WORD_1
	v_mfma_f32_16x16x32_f16 a[0:3], v[8:11], v[20:23], a[0:3]
	v_add_f32_e64 v12, v12, -v16
	v_add_f32_e64 v13, v13, -v17
	v_cvt_pk_f16_f32 v26, v12, v13
	v_cvt_f32_f16_e32 v12, v21
	v_cvt_f32_f16_sdwa v13, v21 dst_sel:DWORD dst_unused:UNUSED_PAD src0_sel:WORD_1
	v_pk_add_f32 v[12:13], v[18:19], v[12:13] neg_lo:[0,1] neg_hi:[0,1]
	s_nop 0
	v_cvt_pk_f16_f32 v25, v12, v13
	v_cvt_f32_f16_e32 v12, v23
	v_cvt_f32_f16_sdwa v13, v23 dst_sel:DWORD dst_unused:UNUSED_PAD src0_sel:WORD_1
	v_pk_add_f32 v[12:13], v[14:15], v[12:13] neg_lo:[0,1] neg_hi:[0,1]
	s_nop 0
	v_cvt_pk_f16_f32 v27, v12, v13
	s_nop 1
	v_mfma_f32_16x16x32_f16 a[0:3], v[8:11], v[24:27], a[0:3]
	global_load_dwordx4 v[8:11], v[6:7], off
	global_load_dwordx4 v[12:15], v[4:5], off offset:-128
	global_load_dwordx4 v[16:19], v[4:5], off offset:-144
	s_waitcnt vmcnt(1)
	v_cvt_pk_f16_f32 v22, v12, v13
	s_waitcnt vmcnt(0)
	v_cvt_f16_f32_e32 v3, v16
	v_cvt_f16_f32_e32 v21, v17
	v_cvt_pk_f16_f32 v20, v16, v17
	v_cvt_pk_f16_f32 v23, v14, v15
	v_cvt_f32_f16_e32 v3, v3
	v_sub_f32_e32 v3, v16, v3
	v_cvt_f32_f16_e32 v16, v21
	v_cvt_pk_f16_f32 v21, v18, v19
	v_sub_f32_e32 v16, v17, v16
	v_cvt_pk_f16_f32 v24, v3, v16
	v_cvt_f32_f16_e32 v16, v22
	v_cvt_f32_f16_sdwa v17, v22 dst_sel:DWORD dst_unused:UNUSED_PAD src0_sel:WORD_1
	v_mfma_f32_16x16x32_f16 a[0:3], v[8:11], v[20:23], a[0:3]
	v_add_f32_e64 v12, v12, -v16
	v_add_f32_e64 v13, v13, -v17
	v_cvt_pk_f16_f32 v26, v12, v13
	v_cvt_f32_f16_e32 v12, v21
	v_cvt_f32_f16_sdwa v13, v21 dst_sel:DWORD dst_unused:UNUSED_PAD src0_sel:WORD_1
	v_pk_add_f32 v[12:13], v[18:19], v[12:13] neg_lo:[0,1] neg_hi:[0,1]
	s_nop 0
	v_cvt_pk_f16_f32 v25, v12, v13
	v_cvt_f32_f16_e32 v12, v23
	v_cvt_f32_f16_sdwa v13, v23 dst_sel:DWORD dst_unused:UNUSED_PAD src0_sel:WORD_1
	v_pk_add_f32 v[12:13], v[14:15], v[12:13] neg_lo:[0,1] neg_hi:[0,1]
	s_nop 0
	v_cvt_pk_f16_f32 v27, v12, v13
	s_nop 1
	v_mfma_f32_16x16x32_f16 a[0:3], v[8:11], v[24:27], a[0:3]
	global_load_dwordx4 v[8:11], v[6:7], off offset:1024
	global_load_dwordx4 v[12:15], v[4:5], off
	global_load_dwordx4 v[16:19], v[4:5], off offset:-16
	v_lshl_add_u64 v[4:5], v[4:5], 0, s[0:1]
	v_lshl_add_u64 v[6:7], v[6:7], 0, s[2:3]
	s_waitcnt vmcnt(1)
	v_cvt_pk_f16_f32 v22, v12, v13
	s_waitcnt vmcnt(0)
	v_cvt_f16_f32_e32 v3, v16
	v_cvt_f16_f32_e32 v21, v17
	v_cvt_pk_f16_f32 v20, v16, v17
	v_cvt_pk_f16_f32 v23, v14, v15
	v_cvt_f32_f16_e32 v3, v3
	v_sub_f32_e32 v3, v16, v3
	v_cvt_f32_f16_e32 v16, v21
	v_cvt_pk_f16_f32 v21, v18, v19
	v_sub_f32_e32 v16, v17, v16
	v_cvt_pk_f16_f32 v24, v3, v16
	v_cvt_f32_f16_e32 v16, v22
	v_cvt_f32_f16_sdwa v17, v22 dst_sel:DWORD dst_unused:UNUSED_PAD src0_sel:WORD_1
	v_mfma_f32_16x16x32_f16 a[0:3], v[8:11], v[20:23], a[0:3]
	v_add_f32_e64 v12, v12, -v16
	v_add_f32_e64 v13, v13, -v17
	v_cvt_pk_f16_f32 v26, v12, v13
	v_cvt_f32_f16_e32 v12, v21
	v_cvt_f32_f16_sdwa v13, v21 dst_sel:DWORD dst_unused:UNUSED_PAD src0_sel:WORD_1
	v_pk_add_f32 v[12:13], v[18:19], v[12:13] neg_lo:[0,1] neg_hi:[0,1]
	s_nop 0
	v_cvt_pk_f16_f32 v25, v12, v13
	v_cvt_f32_f16_e32 v12, v23
	v_cvt_f32_f16_sdwa v13, v23 dst_sel:DWORD dst_unused:UNUSED_PAD src0_sel:WORD_1
	v_pk_add_f32 v[12:13], v[14:15], v[12:13] neg_lo:[0,1] neg_hi:[0,1]
	s_nop 0
	v_cvt_pk_f16_f32 v27, v12, v13
	s_nop 1
	v_mfma_f32_16x16x32_f16 a[0:3], v[8:11], v[24:27], a[0:3]
	s_cbranch_scc0 .LBB3_2
	v_lshlrev_b32_e32 v4, 2, v2
	global_load_dword v4, v4, s[8:9]
	v_lshlrev_b32_e32 v0, 2, v0
	v_lshlrev_b32_e32 v5, 4, v1
	v_and_b32_e32 v0, 0xc0, v0
	s_nop 1
	v_accvgpr_read_b32 v10, a0
	v_mov_b32_e32 v1, 0
	v_or3_b32 v0, v0, v5, v2
	v_accvgpr_read_b32 v9, a1
	v_accvgpr_read_b32 v8, a2
	v_accvgpr_read_b32 v3, a3
	v_lshl_add_u64 v[0:1], v[0:1], 2, s[10:11]
	s_waitcnt vmcnt(0)
	v_add_f32_e32 v2, v4, v10
	v_add_f32_e32 v5, v4, v9
	v_add_f32_e32 v6, v4, v8
	v_add_f32_e32 v3, v4, v3
	global_store_dword v[0:1], v2, off
	global_store_dword v[0:1], v5, off offset:64
	global_store_dword v[0:1], v6, off offset:128
	global_store_dword v[0:1], v3, off offset:192
